# GLA chunk loop: q~ fragment reads of O_inter = q~ S_prev run three MFMAs ahead through a four-quad register ring (counted lgkmcnt waits) instead of one LDS round trip per MFMA
# speedup vs baseline: 1.0124x; 1.0071x over previous
; #define LAS __attribute__((address_space(3)))
; __device__ __forceinline__ void gla_unit(LAS unsigned char* lds, const unsigned char* ws, const float* g_onorm, const int b, const int h, const int wv) {
;     ...
;         f32x16 O[2];
; #pragma unroll
;         for (int tt = 0; tt < 2; ++tt)
; #pragma unroll
;             for (int r = 0; r < 16; ++r) O[tt][r] = 0.f;
; #pragma unroll
;         for (int et = 0; et < 4; ++et)
; #pragma unroll
;             for (int s2 = 0; s2 < 2; ++s2) {
;                 const bf16x8 sb = pack8(S[et], s2);
; #pragma unroll
;                 for (int tt = 0; tt < 2; ++tt) {
;                     const bf16x8 aq = ld2x64(qb8 + 32 * tt * QS + (32 * et + 16 * s2) * 2);
;                     O[tt] = __builtin_amdgcn_mfma_f32_32x32x16_bf16(aq, sb, O[tt], 0, 0, 0);
;                 }
;             }
;         __syncthreads();
; #pragma unroll
;         for (int pr = 0; pr < 3; ++pr) {
;             const int st = (pr == 2) ? 1 : 0, tt = (pr == 0) ? 0 : 1;
; #pragma unroll
;             for (int s2 = 0; s2 < 2; ++s2) {
;                 const bf16x8 ax = *(const LAS bf16x8*)(frb + (pr * 2 + s2) * 1024);
;                 const LAS unsigned char* vp = vP + (32 * st + 16 * s2) * VS;
;                 const bf16x8 bv = tr8(vp, vp + 8 * VS);
;                 O[tt] = __builtin_amdgcn_mfma_f32_32x32x16_bf16(ax, bv, O[tt], 0, 0, 0);
;             }
;         }
;         __builtin_amdgcn_sched_barrier(0);
; #pragma unroll
;         for (int tt = 0; tt < 2; ++tt)
; #pragma unroll
;             for (int r = 0; r < 16; ++r) ob[(32 * tt + (r & 3) + 8 * (r >> 2)) * OS] = O[tt][r];
.LBB0_635:
	ds_read2_b64 v[64:67], v222 offset1:2
	v_cvt_pk_bf16_f32 v68, v32, v33
	v_cvt_pk_bf16_f32 v69, v34, v35
	v_cvt_pk_bf16_f32 v70, v36, v37
	v_cvt_pk_bf16_f32 v71, v38, v39
	ds_read2_b64 v[192:195], v222 offset0:4 offset1:6
	v_cvt_pk_bf16_f32 v196, v40, v41
	v_cvt_pk_bf16_f32 v197, v42, v43
	v_cvt_pk_bf16_f32 v198, v44, v45
	s_waitcnt lgkmcnt(1)
	v_mfma_f32_32x32x16_bf16 v[80:95], v[64:67], v[68:71], 0
	ds_read2_b64 v[64:67], v223 offset0:64 offset1:66
	v_cvt_pk_bf16_f32 v199, v46, v47
	s_waitcnt lgkmcnt(1)
	s_nop 0
	v_mfma_f32_32x32x16_bf16 v[80:95], v[192:195], v[196:199], v[80:95]
	ds_read2_b64 v[192:195], v223 offset0:68 offset1:70
	s_waitcnt lgkmcnt(1)
	v_mfma_f32_32x32x16_bf16 v[64:79], v[64:67], v[68:71], 0
	s_waitcnt lgkmcnt(0)
	v_mfma_f32_32x32x16_bf16 v[64:79], v[192:195], v[196:199], v[64:79]
	ds_read2_b64 v[192:195], v222 offset0:8 offset1:10
	ds_read2_b64 v[224:227], v223 offset0:72 offset1:74
	ds_read2_b64 v[232:235], v222 offset0:12 offset1:14
	v_cvt_pk_bf16_f32 v196, v16, v17
	v_cvt_pk_bf16_f32 v197, v18, v19
	v_cvt_pk_bf16_f32 v198, v20, v21
	v_cvt_pk_bf16_f32 v199, v22, v23
	s_waitcnt lgkmcnt(2)
	s_nop 0
	v_mfma_f32_32x32x16_bf16 v[80:95], v[192:195], v[196:199], v[80:95]
	ds_read2_b64 v[236:239], v223 offset0:76 offset1:78
	s_waitcnt lgkmcnt(2)
	v_mfma_f32_32x32x16_bf16 v[64:79], v[224:227], v[196:199], v[64:79]
	ds_read2_b64 v[192:195], v222 offset0:16 offset1:18
	v_cvt_pk_bf16_f32 v196, v24, v25
	v_cvt_pk_bf16_f32 v197, v26, v27
	v_cvt_pk_bf16_f32 v198, v28, v29
	v_cvt_pk_bf16_f32 v199, v30, v31
	s_waitcnt lgkmcnt(2)
	s_nop 0
	v_mfma_f32_32x32x16_bf16 v[80:95], v[232:235], v[196:199], v[80:95]
	ds_read2_b64 v[224:227], v223 offset0:80 offset1:82
	s_waitcnt lgkmcnt(2)
	v_mfma_f32_32x32x16_bf16 v[64:79], v[236:239], v[196:199], v[64:79]
	ds_read2_b64 v[232:235], v222 offset0:20 offset1:22
	v_cvt_pk_bf16_f32 v196, v48, v49
	v_cvt_pk_bf16_f32 v197, v50, v51
	v_cvt_pk_bf16_f32 v198, v52, v53
	v_cvt_pk_bf16_f32 v199, v54, v55
	s_waitcnt lgkmcnt(2)
	s_nop 0
	v_mfma_f32_32x32x16_bf16 v[80:95], v[192:195], v[196:199], v[80:95]
	ds_read2_b64 v[236:239], v223 offset0:84 offset1:86
	s_waitcnt lgkmcnt(2)
	v_mfma_f32_32x32x16_bf16 v[64:79], v[224:227], v[196:199], v[64:79]
	ds_read2_b64 v[192:195], v222 offset0:24 offset1:26
	v_cvt_pk_bf16_f32 v196, v56, v57
	v_cvt_pk_bf16_f32 v197, v58, v59
	v_cvt_pk_bf16_f32 v198, v60, v61
	v_cvt_pk_bf16_f32 v199, v62, v63
	s_waitcnt lgkmcnt(2)
	s_nop 0
	v_mfma_f32_32x32x16_bf16 v[80:95], v[232:235], v[196:199], v[80:95]
	ds_read2_b64 v[224:227], v223 offset0:88 offset1:90
	s_waitcnt lgkmcnt(2)
	v_mfma_f32_32x32x16_bf16 v[64:79], v[236:239], v[196:199], v[64:79]
	ds_read2_b64 v[232:235], v222 offset0:28 offset1:30
	v_cvt_pk_bf16_f32 v196, v0, v1
	v_cvt_pk_bf16_f32 v197, v2, v3
	v_cvt_pk_bf16_f32 v198, v4, v5
	v_cvt_pk_bf16_f32 v199, v6, v7
	s_waitcnt lgkmcnt(2)
	s_nop 0
	v_mfma_f32_32x32x16_bf16 v[80:95], v[192:195], v[196:199], v[80:95]
	ds_read2_b64 v[236:239], v223 offset0:92 offset1:94
	s_waitcnt lgkmcnt(2)
	v_mfma_f32_32x32x16_bf16 v[64:79], v[224:227], v[196:199], v[64:79]
	v_cvt_pk_bf16_f32 v196, v8, v9
	v_cvt_pk_bf16_f32 v197, v10, v11
	v_cvt_pk_bf16_f32 v198, v12, v13
	v_cvt_pk_bf16_f32 v199, v14, v15
	s_waitcnt lgkmcnt(1)
	s_nop 0
	v_mfma_f32_32x32x16_bf16 v[80:95], v[232:235], v[196:199], v[80:95]
	s_waitcnt lgkmcnt(0)
	s_barrier
	v_mfma_f32_32x32x16_bf16 v[64:79], v[236:239], v[196:199], v[64:79]
	ds_read_b128 v[192:195], v206
	ds_read_b64_tr_b16 v[196:197], v218
	ds_read_b64_tr_b16 v[198:199], v218 offset:4608
	ds_read_b128 v[222:225], v206 offset:1024
	ds_read_b64_tr_b16 v[226:227], v218 offset:9216
	ds_read_b64_tr_b16 v[228:229], v218 offset:13824
	s_waitcnt lgkmcnt(3)
	v_mfma_f32_32x32x16_bf16 v[80:95], v[192:195], v[196:199], v[80:95]
	s_waitcnt lgkmcnt(0)
	v_mfma_f32_32x32x16_bf16 v[80:95], v[222:225], v[226:229], v[80:95]
	ds_read_b128 v[192:195], v206 offset:2048
	ds_read_b128 v[222:225], v206 offset:3072
	s_waitcnt lgkmcnt(1)
	v_mfma_f32_32x32x16_bf16 v[64:79], v[192:195], v[196:199], v[64:79]
	s_waitcnt lgkmcnt(0)
	v_mfma_f32_32x32x16_bf16 v[64:79], v[222:225], v[226:229], v[64:79]
	ds_read_b128 v[192:195], v206 offset:4096
	ds_read_b64_tr_b16 v[196:197], v218 offset:18432
	ds_read_b64_tr_b16 v[198:199], v218 offset:23040
	ds_read_b128 v[222:225], v206 offset:5120
	ds_read_b64_tr_b16 v[226:227], v218 offset:27648
	ds_read_b64_tr_b16 v[228:229], v218 offset:32256
	s_waitcnt lgkmcnt(3)
	v_mfma_f32_32x32x16_bf16 v[64:79], v[192:195], v[196:199], v[64:79]
	s_waitcnt lgkmcnt(0)
	v_mfma_f32_32x32x16_bf16 v[64:79], v[222:225], v[226:229], v[64:79]
	ds_write_b32 v207, v80
	ds_write_b32 v207, v81 offset:1040
	ds_write_b32 v207, v82 offset:2080
	ds_write_b32 v207, v83 offset:3120
	ds_write_b32 v207, v84 offset:8320
	ds_write_b32 v207, v85 offset:9360
	ds_write_b32 v207, v86 offset:10400
	ds_write_b32 v207, v87 offset:11440
	ds_write_b32 v207, v88 offset:16640
	ds_write_b32 v207, v89 offset:17680
	ds_write_b32 v207, v90 offset:18720
	ds_write_b32 v207, v91 offset:19760
	ds_write_b32 v207, v92 offset:24960
	ds_write_b32 v207, v93 offset:26000
	ds_write_b32 v207, v94 offset:27040
	ds_write_b32 v207, v95 offset:28080
	ds_write_b32 v207, v64 offset:33280
	ds_write_b32 v207, v65 offset:34320
	ds_write_b32 v207, v66 offset:35360
	ds_write_b32 v207, v67 offset:36400
	ds_write_b32 v207, v68 offset:41600
	ds_write_b32 v207, v69 offset:42640
	ds_write_b32 v207, v70 offset:43680
	ds_write_b32 v207, v71 offset:44720
	ds_write_b32 v207, v72 offset:49920
	ds_write_b32 v207, v73 offset:50960
	ds_write_b32 v207, v74 offset:52000
	ds_write_b32 v207, v75 offset:53040
	ds_write_b32 v207, v76 offset:58240
	ds_write_b32 v207, v77 offset:59280
	ds_write_b32 v207, v78 offset:60320
	ds_write_b32 v207, v79 offset:61360
	ds_read_b128 v[64:67], v205 offset:96
	ds_read_b128 v[68:71], v205 offset:64
	ds_read_b128 v[72:75], v205 offset:32
	ds_read_b128 v[76:79], v205
	s_waitcnt vmcnt(11)
; #define LAS __attribute__((address_space(3)))
; __device__ __forceinline__ void gla_unit(LAS unsigned char* lds, const unsigned char* ws, const float* g_onorm, const int b, const int h, const int wv) {
;     ...
; #pragma unroll
;         for (int et = 0; et < 4; ++et)
; #pragma unroll
;             for (int rg = 0; rg < 4; ++rg) { const f32x4 dl = *(const LAS f32x4*)&decb[32 * et + 8 * rg];
; #pragma unroll
;                 for (int x = 0; x < 4; ++x) S[et][4 * rg + x] *= dl[x]; }
; #pragma unroll
;         for (int ks = 0; ks < 4; ++ks) {
;             const LAS unsigned char* vp = vN + 16 * ks * VS;
;             const bf16x8 bv = tr8(vp, vp + 4 * VS);
; #pragma unroll
;             for (int et = 0; et < 4; ++et) {
;                 const LAS unsigned char* kp = keN + 32 * et * 2 + 16 * ks * ES;
;                 const bf16x8 ak = tr8(kp, kp + 4 * ES);
;                 S[et] = __builtin_amdgcn_mfma_f32_32x32x16_bf16(ak, bv, S[et], 0, 0, 0);
;             }
;         }
;         __syncthreads();
	v_lshlrev_b32_e32 v232, 16, v176
	s_waitcnt lgkmcnt(3)
	v_pk_mul_f32 v[46:47], v[46:47], v[66:67]
	s_waitcnt lgkmcnt(2)
	v_pk_mul_f32 v[42:43], v[42:43], v[70:71]
	v_pk_mul_f32 v[44:45], v[44:45], v[64:65]
	s_waitcnt lgkmcnt(0)
	v_pk_mul_f32 v[34:35], v[34:35], v[78:79]
	v_pk_mul_f32 v[40:41], v[40:41], v[68:69]
	ds_read_b128 v[68:71], v205 offset:192
	ds_read_b128 v[78:81], v205 offset:224
	ds_read_b128 v[64:67], v205 offset:128
	ds_read_b128 v[82:85], v205 offset:160
	v_pk_mul_f32 v[38:39], v[38:39], v[74:75]
	v_pk_mul_f32 v[36:37], v[36:37], v[72:73]
	v_pk_mul_f32 v[32:33], v[32:33], v[76:77]
	s_waitcnt lgkmcnt(2)
	v_pk_mul_f32 v[30:31], v[30:31], v[80:81]
	v_pk_mul_f32 v[26:27], v[26:27], v[70:71]
	s_waitcnt lgkmcnt(0)
	v_pk_mul_f32 v[22:23], v[22:23], v[84:85]
	v_pk_mul_f32 v[18:19], v[18:19], v[66:67]
	v_pk_mul_f32 v[28:29], v[28:29], v[78:79]
	v_pk_mul_f32 v[24:25], v[24:25], v[68:69]
	v_pk_mul_f32 v[20:21], v[20:21], v[82:83]
	ds_read_b128 v[66:69], v205 offset:256
	ds_read_b128 v[70:73], v205 offset:288
	ds_read_b128 v[74:77], v205 offset:320
	ds_read_b128 v[78:81], v205 offset:352
	ds_read_b64_tr_b16 v[82:83], v219
	ds_read_b64_tr_b16 v[84:85], v219 offset:2304
	ds_read_b64_tr_b16 v[88:89], v220 offset:1280
	ds_read_b64_tr_b16 v[86:87], v220
	ds_read_b64_tr_b16 v[90:91], v220 offset:64
	ds_read_b64_tr_b16 v[192:193], v220 offset:128
	ds_read_b64_tr_b16 v[196:197], v220 offset:192
	ds_read_b64_tr_b16 v[92:93], v220 offset:1344
	ds_read_b64_tr_b16 v[194:195], v220 offset:1408
	ds_read_b64_tr_b16 v[198:199], v220 offset:1472
	ds_read_b64_tr_b16 v[222:223], v219 offset:9216
	ds_read_b64_tr_b16 v[224:225], v219 offset:11520
	s_waitcnt lgkmcnt(8)
	v_mfma_f32_32x32x16_bf16 v[32:47], v[86:89], v[82:85], v[32:47]
	v_mul_f32_e64 v58, v58, v76
	v_mul_f32_e64 v59, v59, v77
	v_mul_f32_e64 v54, v54, v72
	v_mul_f32_e64 v55, v55, v73
	v_mul_f32_e64 v50, v50, v68
	v_mul_f32_e64 v51, v51, v69
	v_pk_mul_f32 v[60:61], v[60:61], v[78:79]
	v_pk_mul_f32 v[56:57], v[56:57], v[74:75]
	ds_read_b128 v[72:75], v205 offset:448
	ds_read_b128 v[76:79], v205 offset:480
	v_pk_mul_f32 v[52:53], v[52:53], v[70:71]
	ds_read_b128 v[68:71], v205 offset:384
	ds_read_b128 v[86:89], v205 offset:416
	v_pk_mul_f32 v[16:17], v[16:17], v[64:65]
	v_pk_mul_f32 v[62:63], v[62:63], v[80:81]
	v_pk_mul_f32 v[48:49], v[48:49], v[66:67]
	s_waitcnt lgkmcnt(2)
	v_pk_mul_f32 v[14:15], v[14:15], v[78:79]
	v_pk_mul_f32 v[10:11], v[10:11], v[74:75]
	s_waitcnt lgkmcnt(0)
	v_pk_mul_f32 v[6:7], v[6:7], v[88:89]
	v_pk_mul_f32 v[2:3], v[2:3], v[70:71]
	v_pk_mul_f32 v[12:13], v[12:13], v[76:77]
	v_pk_mul_f32 v[8:9], v[8:9], v[72:73]
	v_pk_mul_f32 v[4:5], v[4:5], v[86:87]
	v_pk_mul_f32 v[0:1], v[0:1], v[68:69]
	v_mfma_f32_32x32x16_bf16 v[16:31], v[90:93], v[82:85], v[16:31]
	ds_read_b64_tr_b16 v[66:67], v220 offset:6400
	ds_read_b64_tr_b16 v[64:65], v220 offset:5120
	ds_read_b64_tr_b16 v[68:69], v220 offset:5184
	ds_read_b64_tr_b16 v[72:73], v220 offset:5248
	ds_read_b64_tr_b16 v[76:77], v220 offset:5312
	ds_read_b64_tr_b16 v[70:71], v220 offset:6464
	ds_read_b64_tr_b16 v[74:75], v220 offset:6528
	ds_read_b64_tr_b16 v[78:79], v220 offset:6592
	v_and_b32_e32 v233, 0xffff0000, v176
	s_mov_b32 s2, 0x4e1c8000
	s_add_i32 s60, s60, 2
	v_lshl_add_u64 v[184:185], v[184:185], 0, s[68:69]
	v_lshl_add_u64 v[188:189], v[188:189], 0, s[70:71]
	s_cmp_lt_u32 s66, 30
	v_mfma_f32_32x32x16_bf16 v[48:63], v[192:195], v[82:85], v[48:63]
	v_lshl_add_u64 v[190:191], v[190:191], 0, s[68:69]
	v_mfma_f32_32x32x16_bf16 v[0:15], v[196:199], v[82:85], v[0:15]
	s_waitcnt lgkmcnt(6)
	v_mfma_f32_32x32x16_bf16 v[32:47], v[64:67], v[222:225], v[32:47]
	s_waitcnt lgkmcnt(2)
	v_mfma_f32_32x32x16_bf16 v[16:31], v[68:71], v[222:225], v[16:31]
	s_waitcnt lgkmcnt(1)
	v_mfma_f32_32x32x16_bf16 v[48:63], v[72:75], v[222:225], v[48:63]
	s_waitcnt lgkmcnt(0)
	v_mfma_f32_32x32x16_bf16 v[0:15], v[76:79], v[222:225], v[0:15]
	ds_read_b64_tr_b16 v[64:65], v219 offset:18432
	ds_read_b64_tr_b16 v[66:67], v219 offset:20736
	ds_read_b64_tr_b16 v[70:71], v220 offset:11520
	ds_read_b64_tr_b16 v[68:69], v220 offset:10240
	ds_read_b64_tr_b16 v[72:73], v220 offset:10304
	ds_read_b64_tr_b16 v[76:77], v220 offset:10368
	ds_read_b64_tr_b16 v[80:81], v220 offset:10432
	ds_read_b64_tr_b16 v[74:75], v220 offset:11584
	ds_read_b64_tr_b16 v[78:79], v220 offset:11648
	ds_read_b64_tr_b16 v[82:83], v220 offset:11712
	ds_read_b64_tr_b16 v[84:85], v219 offset:27648
	ds_read_b64_tr_b16 v[86:87], v219 offset:29952
	s_waitcnt lgkmcnt(8)
	v_mfma_f32_32x32x16_bf16 v[32:47], v[68:71], v[64:67], v[32:47]
	ds_read_b64_tr_b16 v[68:69], v220 offset:16640
	s_waitcnt lgkmcnt(5)
	v_mfma_f32_32x32x16_bf16 v[16:31], v[72:75], v[64:67], v[16:31]
	s_waitcnt lgkmcnt(4)
	v_mfma_f32_32x32x16_bf16 v[48:63], v[76:79], v[64:67], v[48:63]
	s_waitcnt lgkmcnt(3)
	v_mfma_f32_32x32x16_bf16 v[0:15], v[80:83], v[64:67], v[0:15]
	ds_read_b64_tr_b16 v[66:67], v220 offset:15360
	ds_read_b64_tr_b16 v[70:71], v220 offset:15424
	ds_read_b64_tr_b16 v[74:75], v220 offset:15488
	ds_read_b64_tr_b16 v[78:79], v220 offset:15552
	ds_read_b64_tr_b16 v[72:73], v220 offset:16704
	ds_read_b64_tr_b16 v[76:77], v220 offset:16768
	ds_read_b64_tr_b16 v[80:81], v220 offset:16832
	s_waitcnt lgkmcnt(0)
	s_barrier
; #define LAS __attribute__((address_space(3)))
; __device__ __forceinline__ unsigned cvt_pk_bf16(float lo, float hi) { const bf16x2_t r = __builtin_convertvector((f32x2_t){lo, hi}, bf16x2_t); return __builtin_bit_cast(unsigned, r); }
; __device__ __forceinline__ float bf_lo(unsigned w) { return __uint_as_float(w << 16); }
; __device__ __forceinline__ float bf_hi(unsigned w) { return __uint_as_float(w & 0xffff0000u); }
; __device__ __forceinline__ void gla_unit(LAS unsigned char* lds, const unsigned char* ws, const float* g_onorm, const int b, const int h, const int wv) {
;     ...
;         {
;             const int t = tid >> 3, g8 = tid & 7;
;             float ov[32]; float ss = 0.f;
; #pragma unroll
;             for (int x = 0; x < 8; ++x) { const f32x4 v = *(const LAS f32x4*)&obuf[t * OS + 32 * g8 + 4 * x]; ov[4 * x] = v[0]; ov[4 * x + 1] = v[1]; ov[4 * x + 2] = v[2]; ov[4 * x + 3] = v[3];
;                 ss += v[0] * v[0] + v[1] * v[1] + v[2] * v[2] + v[3] * v[3]; }
;             ss += __builtin_bit_cast(float, __builtin_amdgcn_ds_swizzle(__builtin_bit_cast(int, ss), (1 << 10) | 0x1F)); ss += __builtin_bit_cast(float, __builtin_amdgcn_ds_swizzle(__builtin_bit_cast(int, ss), (2 << 10) | 0x1F));
;             ss += __builtin_bit_cast(float, __builtin_amdgcn_ds_swizzle(__builtin_bit_cast(int, ss), (4 << 10) | 0x1F));
;             const float rstd = __builtin_amdgcn_rsqf(ss * (1.0f / 256.0f) + EPSV);
;             bf16_t* mp = mix + (t0 + t) * DM + 1024 + h * 256 + 32 * g8;
; #pragma unroll
;             for (int x = 0; x < 4; ++x) {
;                 const u32x4 og = ogr[x];
;                 const f32x4 g0 = *(const LAS f32x4*)&gon[32 * g8 + 8 * x], g1 = *(const LAS f32x4*)&gon[32 * g8 + 8 * x + 4];
;                 const float gg2[8] = {g0[0], g0[1], g0[2], g0[3], g1[0], g1[1], g1[2], g1[3]};
;                 float res[8];
; #pragma unroll
;                 for (int y = 0; y < 4; ++y) { const float a0 = bf_lo(og[y]), a1 = bf_hi(og[y]);
;                     res[2 * y] = ov[8 * x + 2 * y] * rstd * gg2[2 * y] * a0;
;                     res[2 * y + 1] = ov[8 * x + 2 * y + 1] * rstd * gg2[2 * y + 1] * a1; }
;                 u32x4 wv4; wv4[0] = cvt_pk_bf16(res[0], res[1]); wv4[1] = cvt_pk_bf16(res[2], res[3]); wv4[2] = cvt_pk_bf16(res[4], res[5]); wv4[3] = cvt_pk_bf16(res[6], res[7]);
;                 *(u32x4*)(mp + 8 * x) = wv4;
;             }
	v_mfma_f32_32x32x16_bf16 v[32:47], v[66:69], v[84:87], v[32:47]
	ds_read_b128 v[64:67], v221
	ds_read_b128 v[88:91], v221 offset:16
	ds_read_b128 v[92:95], v221 offset:32
	ds_read_b128 v[192:195], v221 offset:48
	s_waitcnt lgkmcnt(3)
	v_mul_f32_e32 v68, v65, v65
	s_waitcnt lgkmcnt(2)
	v_mul_f32_e32 v69, v89, v89
	v_fmac_f32_e32 v68, v64, v64
	v_fmac_f32_e32 v69, v88, v88
	v_fmac_f32_e32 v68, v66, v66
	v_fmac_f32_e32 v69, v90, v90
	v_mfma_f32_32x32x16_bf16 v[16:31], v[70:73], v[84:87], v[16:31]
	v_fmac_f32_e32 v68, v67, v67
	v_fmac_f32_e32 v69, v91, v91
	s_waitcnt lgkmcnt(1)
	v_mov_b32_e32 v70, v93
	s_waitcnt lgkmcnt(0)
	v_mov_b32_e32 v71, v193
	v_add_f32_e32 v222, v68, v69
	v_mov_b32_e32 v68, v92
	v_mov_b32_e32 v69, v192
	v_pk_mul_f32 v[70:71], v[70:71], v[70:71]
	v_mov_b32_e32 v82, v95
	v_pk_fma_f32 v[68:69], v[68:69], v[68:69], v[70:71]
	v_mov_b32_e32 v70, v94
	v_mov_b32_e32 v71, v194
	v_pk_fma_f32 v[72:73], v[70:71], v[70:71], v[68:69]
	ds_read_b128 v[68:71], v221 offset:64
	ds_read_b128 v[196:199], v221 offset:80
	v_mov_b32_e32 v83, v195
	v_pk_fma_f32 v[72:73], v[82:83], v[82:83], v[72:73]
	v_mfma_f32_32x32x16_bf16 v[48:63], v[74:77], v[84:87], v[48:63]
	v_add_f32_e32 v72, v222, v72
	s_waitcnt lgkmcnt(1)
	v_mov_b32_e32 v82, v69
	s_waitcnt lgkmcnt(0)
	v_mov_b32_e32 v83, v197
	ds_read_b128 v[222:225], v221 offset:96
	ds_read_b128 v[226:229], v221 offset:112
	v_add_f32_e32 v230, v72, v73
	v_mov_b32_e32 v72, v68
	v_mov_b32_e32 v73, v196
	v_pk_mul_f32 v[82:83], v[82:83], v[82:83]
	v_mfma_f32_32x32x16_bf16 v[0:15], v[78:81], v[84:87], v[0:15]
	v_fma_f32 v72, v72, v72, v82
	v_fma_f32 v73, v73, v73, v83
	v_mov_b32_e32 v82, v70
	v_mov_b32_e32 v83, v198
	v_fma_f32 v72, v82, v82, v72
	v_fma_f32 v73, v83, v83, v73
	v_mov_b32_e32 v82, v71
	v_mov_b32_e32 v83, v199
	v_pk_fma_f32 v[72:73], v[82:83], v[82:83], v[72:73]
	s_waitcnt lgkmcnt(1)
	v_mov_b32_e32 v82, v223
	v_add_f32_e32 v72, v230, v72
	s_waitcnt lgkmcnt(0)
	v_mov_b32_e32 v83, v227
	v_add_f32_e32 v230, v72, v73
	v_mov_b32_e32 v72, v222
	v_mov_b32_e32 v73, v226
	v_pk_mul_f32 v[82:83], v[82:83], v[82:83]
	s_nop 0
	v_pk_fma_f32 v[72:73], v[72:73], v[72:73], v[82:83]
	v_mov_b32_e32 v82, v224
	v_mov_b32_e32 v83, v228
	v_pk_fma_f32 v[72:73], v[82:83], v[82:83], v[72:73]
	v_mov_b32_e32 v82, v225
	v_mov_b32_e32 v83, v229
	v_pk_fma_f32 v[72:73], v[82:83], v[82:83], v[72:73]
	s_nop 0
	v_add_f32_e32 v72, v230, v72
	v_add_f32_e32 v72, v72, v73
	ds_swizzle_b32 v73, v72 offset:swizzle(SWAP,1)
	s_waitcnt lgkmcnt(0)
	v_add_f32_e32 v72, v72, v73
	ds_swizzle_b32 v73, v72 offset:swizzle(SWAP,2)
	s_waitcnt lgkmcnt(0)
	v_add_f32_e32 v72, v72, v73
	ds_swizzle_b32 v73, v72 offset:swizzle(SWAP,4)
	s_waitcnt lgkmcnt(0)
	v_add_f32_e32 v72, v72, v73
	v_fmamk_f32 v72, v72, 0x3b800000, v181
	v_rsq_f32_e32 v230, v72
	ds_read_b128 v[72:75], v208
	ds_read_b128 v[76:79], v208 offset:16
	ds_read_b128 v[80:83], v208 offset:32
	ds_read_b128 v[84:87], v208 offset:48
	v_pk_mul_f32 v[64:65], v[64:65], v[230:231] op_sel_hi:[1,0]
	v_pk_mul_f32 v[66:67], v[66:67], v[230:231] op_sel_hi:[1,0]
	s_waitcnt lgkmcnt(3)
	v_pk_mul_f32 v[64:65], v[72:73], v[64:65]
	v_lshlrev_b32_e32 v72, 16, v177
	v_and_b32_e32 v73, 0xffff0000, v177
	v_pk_mul_f32 v[66:67], v[74:75], v[66:67]
	v_pk_mul_f32 v[74:75], v[88:89], v[230:231] op_sel_hi:[1,0]
	v_pk_mul_f32 v[66:67], v[66:67], v[72:73]
	v_lshlrev_b32_e32 v72, 16, v178
	v_and_b32_e32 v73, 0xffff0000, v178
	s_waitcnt lgkmcnt(2)
	v_pk_mul_f32 v[74:75], v[76:77], v[74:75]
	v_pk_mul_f32 v[76:77], v[90:91], v[230:231] op_sel_hi:[1,0]
	v_pk_mul_f32 v[72:73], v[74:75], v[72:73]
	v_lshlrev_b32_e32 v74, 16, v179
	v_and_b32_e32 v75, 0xffff0000, v179
	v_pk_mul_f32 v[76:77], v[78:79], v[76:77]
	v_pk_mul_f32 v[64:65], v[64:65], v[232:233]
	v_pk_mul_f32 v[74:75], v[76:77], v[74:75]
	v_add_co_u32_e32 v76, vcc, s2, v200
	v_cvt_pk_bf16_f32 v64, v64, v65
	v_cvt_pk_bf16_f32 v65, v66, v67
	v_cvt_pk_bf16_f32 v66, v72, v73
	v_cvt_pk_bf16_f32 v67, v74, v75
	v_addc_co_u32_e32 v77, vcc, 0, v201, vcc
	global_store_dwordx4 v[76:77], v[64:67], off offset:2048
	v_pk_mul_f32 v[72:73], v[94:95], v[230:231] op_sel_hi:[1,0]
	v_pk_mul_f32 v[74:75], v[192:193], v[230:231] op_sel_hi:[1,0]
	v_pk_mul_f32 v[66:67], v[92:93], v[230:231] op_sel_hi:[1,0]
	s_waitcnt vmcnt(9)
; #define LAS __attribute__((address_space(3)))
; __device__ __forceinline__ unsigned cvt_pk_bf16(float lo, float hi) { const bf16x2_t r = __builtin_convertvector((f32x2_t){lo, hi}, bf16x2_t); return __builtin_bit_cast(unsigned, r); }
; __device__ __forceinline__ float bf_lo(unsigned w) { return __uint_as_float(w << 16); }
; __device__ __forceinline__ float bf_hi(unsigned w) { return __uint_as_float(w & 0xffff0000u); }
; __device__ __forceinline__ void gla_unit(LAS unsigned char* lds, const unsigned char* ws, const float* g_onorm, const int b, const int h, const int wv) {
;     ...
; #pragma unroll
;             for (int x = 0; x < 4; ++x) {
;                 const u32x4 og = ogr[x];
;                 const f32x4 g0 = *(const LAS f32x4*)&gon[32 * g8 + 8 * x], g1 = *(const LAS f32x4*)&gon[32 * g8 + 8 * x + 4];
;                 const float gg2[8] = {g0[0], g0[1], g0[2], g0[3], g1[0], g1[1], g1[2], g1[3]};
;                 float res[8];
; #pragma unroll
;                 for (int y = 0; y < 4; ++y) { const float a0 = bf_lo(og[y]), a1 = bf_hi(og[y]);
;                     res[2 * y] = ov[8 * x + 2 * y] * rstd * gg2[2 * y] * a0;
;                     res[2 * y + 1] = ov[8 * x + 2 * y + 1] * rstd * gg2[2 * y + 1] * a1; }
;                 u32x4 wv4; wv4[0] = cvt_pk_bf16(res[0], res[1]); wv4[1] = cvt_pk_bf16(res[2], res[3]); wv4[2] = cvt_pk_bf16(res[4], res[5]); wv4[3] = cvt_pk_bf16(res[6], res[7]);
;                 *(u32x4*)(mp + 8 * x) = wv4;
;             }
	v_lshlrev_b32_e32 v64, 16, v172
	v_and_b32_e32 v65, 0xffff0000, v172
	s_waitcnt lgkmcnt(1)
	v_pk_mul_f32 v[66:67], v[80:81], v[66:67]
	v_pk_mul_f32 v[72:73], v[82:83], v[72:73]
	v_pk_mul_f32 v[64:65], v[66:67], v[64:65]
	v_lshlrev_b32_e32 v66, 16, v173
	v_and_b32_e32 v67, 0xffff0000, v173
	v_pk_mul_f32 v[66:67], v[72:73], v[66:67]
	v_lshlrev_b32_e32 v72, 16, v174
	v_and_b32_e32 v73, 0xffff0000, v174
	s_waitcnt lgkmcnt(0)
	v_pk_mul_f32 v[74:75], v[84:85], v[74:75]
	v_pk_mul_f32 v[78:79], v[194:195], v[230:231] op_sel_hi:[1,0]
	v_pk_mul_f32 v[72:73], v[74:75], v[72:73]
	v_lshlrev_b32_e32 v74, 16, v175
	v_and_b32_e32 v75, 0xffff0000, v175
	v_pk_mul_f32 v[78:79], v[86:87], v[78:79]
	v_cvt_pk_bf16_f32 v64, v64, v65
	v_pk_mul_f32 v[74:75], v[78:79], v[74:75]
	v_cvt_pk_bf16_f32 v65, v66, v67
	v_cvt_pk_bf16_f32 v66, v72, v73
	v_cvt_pk_bf16_f32 v67, v74, v75
	global_store_dwordx4 v[76:77], v[64:67], off offset:2064
	ds_read_b128 v[64:67], v208 offset:64
	ds_read_b128 v[72:75], v208 offset:80
	v_pk_mul_f32 v[68:69], v[68:69], v[230:231] op_sel_hi:[1,0]
	v_pk_mul_f32 v[70:71], v[70:71], v[230:231] op_sel_hi:[1,0]
	v_lshlrev_b32_e32 v78, 16, v168
	s_waitcnt lgkmcnt(1)
	v_pk_mul_f32 v[64:65], v[64:65], v[68:69]
	v_lshlrev_b32_e32 v68, 16, v169
	v_and_b32_e32 v69, 0xffff0000, v169
	v_pk_mul_f32 v[66:67], v[66:67], v[70:71]
	v_pk_mul_f32 v[70:71], v[196:197], v[230:231] op_sel_hi:[1,0]
	v_pk_mul_f32 v[66:67], v[66:67], v[68:69]
	v_lshlrev_b32_e32 v68, 16, v170
	v_and_b32_e32 v69, 0xffff0000, v170
	s_waitcnt lgkmcnt(0)
	v_pk_mul_f32 v[70:71], v[72:73], v[70:71]
	v_pk_mul_f32 v[72:73], v[198:199], v[230:231] op_sel_hi:[1,0]
	v_and_b32_e32 v79, 0xffff0000, v168
	v_pk_mul_f32 v[68:69], v[70:71], v[68:69]
	v_lshlrev_b32_e32 v70, 16, v171
	v_and_b32_e32 v71, 0xffff0000, v171
	v_pk_mul_f32 v[72:73], v[74:75], v[72:73]
	v_pk_mul_f32 v[64:65], v[64:65], v[78:79]
	v_pk_mul_f32 v[70:71], v[72:73], v[70:71]
	v_cvt_pk_bf16_f32 v64, v64, v65
	v_cvt_pk_bf16_f32 v65, v66, v67
	v_cvt_pk_bf16_f32 v66, v68, v69
	v_cvt_pk_bf16_f32 v67, v70, v71
	global_store_dwordx4 v[76:77], v[64:67], off offset:2080
	ds_read_b128 v[64:67], v208 offset:96
	ds_read_b128 v[68:71], v208 offset:112
	v_pk_mul_f32 v[74:75], v[222:223], v[230:231] op_sel_hi:[1,0]
	v_lshlrev_b32_e32 v72, 16, v164
	v_and_b32_e32 v73, 0xffff0000, v164
	s_waitcnt lgkmcnt(1)
	v_pk_mul_f32 v[64:65], v[74:75], v[64:65]
	v_pk_mul_f32 v[74:75], v[224:225], v[230:231] op_sel_hi:[1,0]
	v_pk_mul_f32 v[64:65], v[64:65], v[72:73]
	v_lshlrev_b32_e32 v72, 16, v165
	v_and_b32_e32 v73, 0xffff0000, v165
	v_pk_mul_f32 v[66:67], v[74:75], v[66:67]
	v_pk_mul_f32 v[74:75], v[226:227], v[230:231] op_sel_hi:[1,0]
	v_pk_mul_f32 v[66:67], v[66:67], v[72:73]
	v_lshlrev_b32_e32 v72, 16, v166
	v_and_b32_e32 v73, 0xffff0000, v166
	s_waitcnt lgkmcnt(0)
	v_pk_mul_f32 v[68:69], v[74:75], v[68:69]
	v_pk_mul_f32 v[74:75], v[228:229], v[230:231] op_sel_hi:[1,0]
	v_pk_mul_f32 v[68:69], v[68:69], v[72:73]
	v_lshlrev_b32_e32 v72, 16, v167
	v_and_b32_e32 v73, 0xffff0000, v167
	v_pk_mul_f32 v[70:71], v[74:75], v[70:71]
	s_mov_b64 s[2:3], 0x40000
	v_pk_mul_f32 v[70:71], v[70:71], v[72:73]
	v_lshl_add_u64 v[182:183], v[182:183], 0, s[2:3]
	s_mov_b64 s[2:3], 0x8000
	v_cvt_pk_bf16_f32 v64, v64, v65
	v_cvt_pk_bf16_f32 v65, v66, v67
	v_cvt_pk_bf16_f32 v66, v68, v69
	v_cvt_pk_bf16_f32 v67, v70, v71
	v_lshl_add_u64 v[186:187], v[186:187], 0, s[2:3]
	global_store_dwordx4 v[76:77], v[64:67], off offset:2096
	s_cbranch_scc0 .LBB0_655

; #define LAS __attribute__((address_space(3)))
; __device__ __forceinline__ void gla_unit(LAS unsigned char* lds, const unsigned char* ws, const float* g_onorm, const int b, const int h, const int wv) {
;     ...
;         f32x16 O[2];
; #pragma unroll
;         for (int tt = 0; tt < 2; ++tt)
; #pragma unroll
;             for (int r = 0; r < 16; ++r) O[tt][r] = 0.f;
; #pragma unroll
;         for (int et = 0; et < 4; ++et)
; #pragma unroll
;             for (int s2 = 0; s2 < 2; ++s2) {
;                 const bf16x8 sb = pack8(S[et], s2);
; #pragma unroll
;                 for (int tt = 0; tt < 2; ++tt) {
;                     const bf16x8 aq = ld2x64(qb8 + 32 * tt * QS + (32 * et + 16 * s2) * 2);
;                     O[tt] = __builtin_amdgcn_mfma_f32_32x32x16_bf16(aq, sb, O[tt], 0, 0, 0);
;                 }
;             }
;         __syncthreads();
; #pragma unroll
;         for (int pr = 0; pr < 3; ++pr) {
;             const int st = (pr == 2) ? 1 : 0, tt = (pr == 0) ? 0 : 1;
; #pragma unroll
;             for (int s2 = 0; s2 < 2; ++s2) {
;                 const bf16x8 ax = *(const LAS bf16x8*)(frb + (pr * 2 + s2) * 1024);
;                 const LAS unsigned char* vp = vP + (32 * st + 16 * s2) * VS;
;                 const bf16x8 bv = tr8(vp, vp + 8 * VS);
;                 O[tt] = __builtin_amdgcn_mfma_f32_32x32x16_bf16(ax, bv, O[tt], 0, 0, 0);
;             }
;         }
;         __builtin_amdgcn_sched_barrier(0);
; #pragma unroll
;         for (int tt = 0; tt < 2; ++tt)
; #pragma unroll
;             for (int r = 0; r < 16; ++r) ob[(32 * tt + (r & 3) + 8 * (r >> 2)) * OS] = O[tt][r];
.LBB0_646:
	v_add_u32_e32 v222, v203, v202
	ds_read2_b64 v[64:67], v222 offset1:2
	v_cvt_pk_bf16_f32 v68, v32, v33
	v_cvt_pk_bf16_f32 v69, v34, v35
	v_cvt_pk_bf16_f32 v70, v36, v37
	v_cvt_pk_bf16_f32 v71, v38, v39
	v_add_u32_e32 v223, 0x2000, v222
	ds_read2_b64 v[228:231], v222 offset0:4 offset1:6
	v_cvt_pk_bf16_f32 v232, v40, v41
	v_cvt_pk_bf16_f32 v233, v42, v43
	s_waitcnt lgkmcnt(1)
	v_mfma_f32_32x32x16_bf16 v[80:95], v[64:67], v[68:71], 0
	ds_read2_b64 v[64:67], v223 offset0:64 offset1:66
	v_cvt_pk_bf16_f32 v234, v44, v45
	v_cvt_pk_bf16_f32 v235, v46, v47
	s_waitcnt lgkmcnt(1)
	s_nop 0
	v_mfma_f32_32x32x16_bf16 v[80:95], v[228:231], v[232:235], v[80:95]
	ds_read2_b64 v[228:231], v223 offset0:68 offset1:70
	s_waitcnt lgkmcnt(1)
	v_mfma_f32_32x32x16_bf16 v[64:79], v[64:67], v[68:71], 0
	s_waitcnt lgkmcnt(0)
	v_mfma_f32_32x32x16_bf16 v[64:79], v[228:231], v[232:235], v[64:79]
	ds_read2_b64 v[228:231], v222 offset0:8 offset1:10
	ds_read2_b64 v[236:239], v223 offset0:72 offset1:74
	ds_read2_b64 v[240:243], v222 offset0:12 offset1:14
	v_cvt_pk_bf16_f32 v232, v16, v17
	v_cvt_pk_bf16_f32 v233, v18, v19
	v_cvt_pk_bf16_f32 v234, v20, v21
	v_cvt_pk_bf16_f32 v235, v22, v23
	s_waitcnt lgkmcnt(2)
	s_nop 0
	v_mfma_f32_32x32x16_bf16 v[80:95], v[228:231], v[232:235], v[80:95]
	ds_read2_b64 v[248:251], v223 offset0:76 offset1:78
	s_waitcnt lgkmcnt(2)
	v_mfma_f32_32x32x16_bf16 v[64:79], v[236:239], v[232:235], v[64:79]
	ds_read2_b64 v[228:231], v222 offset0:16 offset1:18
	v_cvt_pk_bf16_f32 v232, v24, v25
	v_cvt_pk_bf16_f32 v233, v26, v27
	v_cvt_pk_bf16_f32 v234, v28, v29
	v_cvt_pk_bf16_f32 v235, v30, v31
	s_waitcnt lgkmcnt(2)
	s_nop 0
	v_mfma_f32_32x32x16_bf16 v[80:95], v[240:243], v[232:235], v[80:95]
	ds_read2_b64 v[236:239], v223 offset0:80 offset1:82
	s_waitcnt lgkmcnt(2)
	v_mfma_f32_32x32x16_bf16 v[64:79], v[248:251], v[232:235], v[64:79]
	ds_read2_b64 v[240:243], v222 offset0:20 offset1:22
	v_cvt_pk_bf16_f32 v232, v48, v49
	v_cvt_pk_bf16_f32 v233, v50, v51
	v_cvt_pk_bf16_f32 v234, v52, v53
	v_cvt_pk_bf16_f32 v235, v54, v55
	s_waitcnt lgkmcnt(2)
	s_nop 0
	v_mfma_f32_32x32x16_bf16 v[80:95], v[228:231], v[232:235], v[80:95]
	ds_read2_b64 v[248:251], v223 offset0:84 offset1:86
	s_waitcnt lgkmcnt(2)
	v_mfma_f32_32x32x16_bf16 v[64:79], v[236:239], v[232:235], v[64:79]
	ds_read2_b64 v[228:231], v222 offset0:24 offset1:26
	v_cvt_pk_bf16_f32 v232, v56, v57
	v_cvt_pk_bf16_f32 v233, v58, v59
	v_cvt_pk_bf16_f32 v234, v60, v61
	v_cvt_pk_bf16_f32 v235, v62, v63
	s_waitcnt lgkmcnt(2)
	s_nop 0
	v_mfma_f32_32x32x16_bf16 v[80:95], v[240:243], v[232:235], v[80:95]
	ds_read2_b64 v[236:239], v223 offset0:88 offset1:90
	s_waitcnt lgkmcnt(2)
	v_mfma_f32_32x32x16_bf16 v[64:79], v[248:251], v[232:235], v[64:79]
	ds_read2_b64 v[240:243], v222 offset0:28 offset1:30
	v_cvt_pk_bf16_f32 v232, v0, v1
	v_cvt_pk_bf16_f32 v233, v2, v3
	v_cvt_pk_bf16_f32 v234, v4, v5
	v_cvt_pk_bf16_f32 v235, v6, v7
	s_waitcnt lgkmcnt(2)
	s_nop 0
	v_mfma_f32_32x32x16_bf16 v[80:95], v[228:231], v[232:235], v[80:95]
	ds_read2_b64 v[248:251], v223 offset0:92 offset1:94
	s_waitcnt lgkmcnt(2)
	v_mfma_f32_32x32x16_bf16 v[64:79], v[236:239], v[232:235], v[64:79]
	v_cvt_pk_bf16_f32 v232, v8, v9
	v_cvt_pk_bf16_f32 v233, v10, v11
	v_cvt_pk_bf16_f32 v234, v12, v13
	v_cvt_pk_bf16_f32 v235, v14, v15
	s_waitcnt lgkmcnt(1)
	s_nop 0
	v_mfma_f32_32x32x16_bf16 v[80:95], v[240:243], v[232:235], v[80:95]
	s_waitcnt lgkmcnt(0)
	s_barrier
	v_mfma_f32_32x32x16_bf16 v[64:79], v[248:251], v[232:235], v[64:79]
	ds_read_b128 v[228:231], v206
	ds_read_b64_tr_b16 v[232:233], v218
	ds_read_b64_tr_b16 v[234:235], v218 offset:4608
	ds_read_b128 v[236:239], v206 offset:1024
	ds_read_b64_tr_b16 v[240:241], v218 offset:9216
	ds_read_b64_tr_b16 v[242:243], v218 offset:13824
	s_waitcnt lgkmcnt(3)
	v_mfma_f32_32x32x16_bf16 v[80:95], v[228:231], v[232:235], v[80:95]
	s_waitcnt lgkmcnt(0)
	v_mfma_f32_32x32x16_bf16 v[80:95], v[236:239], v[240:243], v[80:95]
	ds_read_b128 v[228:231], v206 offset:2048
	ds_read_b128 v[236:239], v206 offset:3072
	s_waitcnt lgkmcnt(1)
	v_mfma_f32_32x32x16_bf16 v[64:79], v[228:231], v[232:235], v[64:79]
	s_waitcnt lgkmcnt(0)
	v_mfma_f32_32x32x16_bf16 v[64:79], v[236:239], v[240:243], v[64:79]
	ds_read_b128 v[228:231], v206 offset:4096
	ds_read_b64_tr_b16 v[232:233], v218 offset:18432
	ds_read_b64_tr_b16 v[234:235], v218 offset:23040
	ds_read_b128 v[236:239], v206 offset:5120
	ds_read_b64_tr_b16 v[240:241], v218 offset:27648
	ds_read_b64_tr_b16 v[242:243], v218 offset:32256
	s_waitcnt lgkmcnt(3)
	v_mfma_f32_32x32x16_bf16 v[64:79], v[228:231], v[232:235], v[64:79]
	s_waitcnt lgkmcnt(0)
	v_mfma_f32_32x32x16_bf16 v[64:79], v[236:239], v[240:243], v[64:79]
	ds_write_b32 v207, v80
	ds_write_b32 v207, v81 offset:1040
	ds_write_b32 v207, v82 offset:2080
	ds_write_b32 v207, v83 offset:3120
	ds_write_b32 v207, v84 offset:8320
	ds_write_b32 v207, v85 offset:9360
	ds_write_b32 v207, v86 offset:10400
	ds_write_b32 v207, v87 offset:11440
	ds_write_b32 v207, v88 offset:16640
	ds_write_b32 v207, v89 offset:17680
	ds_write_b32 v207, v90 offset:18720
	ds_write_b32 v207, v91 offset:19760
	ds_write_b32 v207, v92 offset:24960
	ds_write_b32 v207, v93 offset:26000
	ds_write_b32 v207, v94 offset:27040
	ds_write_b32 v207, v95 offset:28080
	ds_write_b32 v207, v64 offset:33280
	ds_write_b32 v207, v65 offset:34320
	ds_write_b32 v207, v66 offset:35360
	ds_write_b32 v207, v67 offset:36400
	ds_write_b32 v207, v68 offset:41600
	ds_write_b32 v207, v69 offset:42640
	ds_write_b32 v207, v70 offset:43680
	ds_write_b32 v207, v71 offset:44720
	ds_write_b32 v207, v72 offset:49920
	ds_write_b32 v207, v73 offset:50960
	ds_write_b32 v207, v74 offset:52000
	ds_write_b32 v207, v75 offset:53040
	ds_write_b32 v207, v76 offset:58240
	ds_write_b32 v207, v77 offset:59280
	ds_write_b32 v207, v78 offset:60320
	ds_write_b32 v207, v79 offset:61360
	ds_read_b128 v[64:67], v205
	ds_read_b128 v[68:71], v205 offset:32
	ds_read_b128 v[72:75], v205 offset:64
	ds_read_b128 v[76:79], v205 offset:96
	s_waitcnt vmcnt(11)
; #define LAS __attribute__((address_space(3)))
; __device__ __forceinline__ void gla_unit(LAS unsigned char* lds, const unsigned char* ws, const float* g_onorm, const int b, const int h, const int wv) {
;     ...
; #pragma unroll
;         for (int et = 0; et < 4; ++et)
; #pragma unroll
;             for (int rg = 0; rg < 4; ++rg) { const f32x4 dl = *(const LAS f32x4*)&decb[32 * et + 8 * rg];
; #pragma unroll
;                 for (int x = 0; x < 4; ++x) S[et][4 * rg + x] *= dl[x]; }
; #pragma unroll
;         for (int ks = 0; ks < 4; ++ks) {
;             const LAS unsigned char* vp = vN + 16 * ks * VS;
;             const bf16x8 bv = tr8(vp, vp + 4 * VS);
; #pragma unroll
;             for (int et = 0; et < 4; ++et) {
;                 const LAS unsigned char* kp = keN + 32 * et * 2 + 16 * ks * ES;
;                 const bf16x8 ak = tr8(kp, kp + 4 * ES);
;                 S[et] = __builtin_amdgcn_mfma_f32_32x32x16_bf16(ak, bv, S[et], 0, 0, 0);
;             }
;         }
;         __syncthreads();
	v_lshlrev_b32_e32 v246, 16, v176
	s_waitcnt lgkmcnt(3)
	v_pk_mul_f32 v[34:35], v[34:35], v[66:67]
	s_waitcnt lgkmcnt(2)
	v_pk_mul_f32 v[38:39], v[38:39], v[70:71]
	s_waitcnt lgkmcnt(1)
	v_pk_mul_f32 v[42:43], v[42:43], v[74:75]
	s_waitcnt lgkmcnt(0)
	v_pk_mul_f32 v[46:47], v[46:47], v[78:79]
	v_pk_mul_f32 v[44:45], v[44:45], v[76:77]
	v_pk_mul_f32 v[40:41], v[40:41], v[72:73]
	v_pk_mul_f32 v[36:37], v[36:37], v[68:69]
	v_pk_mul_f32 v[32:33], v[32:33], v[64:65]
	ds_read_b128 v[64:67], v205 offset:128
	ds_read_b128 v[68:71], v205 offset:160
	ds_read_b128 v[72:75], v205 offset:192
	ds_read_b128 v[76:79], v205 offset:224
	v_and_b32_e32 v247, 0xffff0000, v176
	s_waitcnt lgkmcnt(3)
	v_pk_mul_f32 v[18:19], v[18:19], v[66:67]
	s_waitcnt lgkmcnt(2)
	v_pk_mul_f32 v[22:23], v[22:23], v[70:71]
	s_waitcnt lgkmcnt(1)
	v_pk_mul_f32 v[26:27], v[26:27], v[74:75]
	s_waitcnt lgkmcnt(0)
	v_pk_mul_f32 v[30:31], v[30:31], v[78:79]
	v_pk_mul_f32 v[28:29], v[28:29], v[76:77]
	v_pk_mul_f32 v[24:25], v[24:25], v[72:73]
	v_pk_mul_f32 v[20:21], v[20:21], v[68:69]
	v_pk_mul_f32 v[16:17], v[16:17], v[64:65]
	ds_read_b128 v[64:67], v205 offset:256
	ds_read_b128 v[68:71], v205 offset:288
	ds_read_b128 v[72:75], v205 offset:320
	ds_read_b128 v[76:79], v205 offset:352
	v_lshlrev_b32_e32 v176, 16, v177
	s_waitcnt lgkmcnt(3)
	v_pk_mul_f32 v[50:51], v[50:51], v[66:67]
	s_waitcnt lgkmcnt(2)
	v_pk_mul_f32 v[54:55], v[54:55], v[70:71]
	s_waitcnt lgkmcnt(1)
	v_pk_mul_f32 v[58:59], v[58:59], v[74:75]
	s_waitcnt lgkmcnt(0)
	v_pk_mul_f32 v[62:63], v[62:63], v[78:79]
	v_pk_mul_f32 v[60:61], v[60:61], v[76:77]
	v_pk_mul_f32 v[56:57], v[56:57], v[72:73]
	v_pk_mul_f32 v[52:53], v[52:53], v[68:69]
	v_pk_mul_f32 v[48:49], v[48:49], v[64:65]
	ds_read_b128 v[64:67], v205 offset:384
	ds_read_b128 v[68:71], v205 offset:416
	ds_read_b128 v[72:75], v205 offset:448
	ds_read_b128 v[76:79], v205 offset:480
	v_and_b32_e32 v177, 0xffff0000, v177
	s_waitcnt lgkmcnt(3)
	v_pk_mul_f32 v[2:3], v[2:3], v[66:67]
	s_waitcnt lgkmcnt(2)
	v_pk_mul_f32 v[6:7], v[6:7], v[70:71]
	v_pk_mul_f32 v[4:5], v[4:5], v[68:69]
	v_pk_mul_f32 v[0:1], v[0:1], v[64:65]
	ds_read_b64_tr_b16 v[64:65], v219
	ds_read_b64_tr_b16 v[66:67], v219 offset:2304
	ds_read_b64_tr_b16 v[68:69], v220
	ds_read_b64_tr_b16 v[70:71], v220 offset:1280
	s_waitcnt lgkmcnt(0)
	v_mfma_f32_32x32x16_bf16 v[32:47], v[68:71], v[64:67], v[32:47]
	ds_read_b64_tr_b16 v[68:69], v220 offset:64
	ds_read_b64_tr_b16 v[70:71], v220 offset:1344
	v_mul_f32_e64 v14, v14, v78
	v_mul_f32_e64 v15, v15, v79
	v_mul_f32_e64 v10, v10, v74
	v_mul_f32_e64 v11, v11, v75
	v_pk_mul_f32 v[12:13], v[12:13], v[76:77]
	v_pk_mul_f32 v[8:9], v[8:9], v[72:73]
	s_waitcnt lgkmcnt(0)
	v_mfma_f32_32x32x16_bf16 v[16:31], v[68:71], v[64:67], v[16:31]
	ds_read_b64_tr_b16 v[68:69], v220 offset:128
	ds_read_b64_tr_b16 v[70:71], v220 offset:1408
	s_waitcnt lgkmcnt(0)
	v_mfma_f32_32x32x16_bf16 v[48:63], v[68:71], v[64:67], v[48:63]
	ds_read_b64_tr_b16 v[68:69], v220 offset:192
	ds_read_b64_tr_b16 v[70:71], v220 offset:1472
	s_waitcnt lgkmcnt(0)
	v_mfma_f32_32x32x16_bf16 v[0:15], v[68:71], v[64:67], v[0:15]
	ds_read_b64_tr_b16 v[64:65], v219 offset:9216
	ds_read_b64_tr_b16 v[66:67], v219 offset:11520
	ds_read_b64_tr_b16 v[68:69], v220 offset:5120
	ds_read_b64_tr_b16 v[70:71], v220 offset:6400
	s_waitcnt lgkmcnt(0)
	v_mfma_f32_32x32x16_bf16 v[32:47], v[68:71], v[64:67], v[32:47]
	ds_read_b64_tr_b16 v[68:69], v220 offset:5184
	ds_read_b64_tr_b16 v[70:71], v220 offset:6464
	s_waitcnt lgkmcnt(0)
	v_mfma_f32_32x32x16_bf16 v[16:31], v[68:71], v[64:67], v[16:31]
	ds_read_b64_tr_b16 v[68:69], v220 offset:5248
	ds_read_b64_tr_b16 v[70:71], v220 offset:6528
	s_waitcnt lgkmcnt(0)
	v_mfma_f32_32x32x16_bf16 v[48:63], v[68:71], v[64:67], v[48:63]
	ds_read_b64_tr_b16 v[68:69], v220 offset:5312
	ds_read_b64_tr_b16 v[70:71], v220 offset:6592
	s_waitcnt lgkmcnt(0)
	v_mfma_f32_32x32x16_bf16 v[0:15], v[68:71], v[64:67], v[0:15]
	ds_read_b64_tr_b16 v[64:65], v219 offset:18432
	ds_read_b64_tr_b16 v[66:67], v219 offset:20736
	ds_read_b64_tr_b16 v[68:69], v220 offset:10240
	ds_read_b64_tr_b16 v[70:71], v220 offset:11520
	s_waitcnt lgkmcnt(0)
	v_mfma_f32_32x32x16_bf16 v[32:47], v[68:71], v[64:67], v[32:47]
	ds_read_b64_tr_b16 v[68:69], v220 offset:10304
	ds_read_b64_tr_b16 v[70:71], v220 offset:11584
	s_waitcnt lgkmcnt(0)
	v_mfma_f32_32x32x16_bf16 v[16:31], v[68:71], v[64:67], v[16:31]
	ds_read_b64_tr_b16 v[68:69], v220 offset:10368
	ds_read_b64_tr_b16 v[70:71], v220 offset:11648
	s_waitcnt lgkmcnt(0)
	v_mfma_f32_32x32x16_bf16 v[48:63], v[68:71], v[64:67], v[48:63]
	ds_read_b64_tr_b16 v[68:69], v220 offset:10432
	ds_read_b64_tr_b16 v[70:71], v220 offset:11712
	s_waitcnt lgkmcnt(0)
	v_mfma_f32_32x32x16_bf16 v[0:15], v[68:71], v[64:67], v[0:15]
	ds_read_b64_tr_b16 v[64:65], v219 offset:27648
	ds_read_b64_tr_b16 v[66:67], v219 offset:29952
	ds_read_b64_tr_b16 v[68:69], v220 offset:15360
	ds_read_b64_tr_b16 v[70:71], v220 offset:16640
	s_waitcnt lgkmcnt(0)
	v_mfma_f32_32x32x16_bf16 v[32:47], v[68:71], v[64:67], v[32:47]
	ds_read_b64_tr_b16 v[68:69], v220 offset:15424
	ds_read_b64_tr_b16 v[70:71], v220 offset:16704
	s_waitcnt lgkmcnt(0)
	v_mfma_f32_32x32x16_bf16 v[16:31], v[68:71], v[64:67], v[16:31]
	ds_read_b64_tr_b16 v[68:69], v220 offset:15488
	ds_read_b64_tr_b16 v[70:71], v220 offset:16768
	s_waitcnt lgkmcnt(0)
	v_mfma_f32_32x32x16_bf16 v[48:63], v[68:71], v[64:67], v[48:63]
	ds_read_b64_tr_b16 v[68:69], v220 offset:15552
	ds_read_b64_tr_b16 v[70:71], v220 offset:16832
	s_waitcnt lgkmcnt(0)
	s_barrier
; #define LAS __attribute__((address_space(3)))
; __device__ __forceinline__ unsigned cvt_pk_bf16(float lo, float hi) { const bf16x2_t r = __builtin_convertvector((f32x2_t){lo, hi}, bf16x2_t); return __builtin_bit_cast(unsigned, r); }
; __device__ __forceinline__ float bf_lo(unsigned w) { return __uint_as_float(w << 16); }
; __device__ __forceinline__ float bf_hi(unsigned w) { return __uint_as_float(w & 0xffff0000u); }
; __device__ __forceinline__ void gla_unit(LAS unsigned char* lds, const unsigned char* ws, const float* g_onorm, const int b, const int h, const int wv) {
;     ...
;         {
;             const int t = tid >> 3, g8 = tid & 7;
;             float ov[32]; float ss = 0.f;
; #pragma unroll
;             for (int x = 0; x < 8; ++x) { const f32x4 v = *(const LAS f32x4*)&obuf[t * OS + 32 * g8 + 4 * x]; ov[4 * x] = v[0]; ov[4 * x + 1] = v[1]; ov[4 * x + 2] = v[2]; ov[4 * x + 3] = v[3];
;                 ss += v[0] * v[0] + v[1] * v[1] + v[2] * v[2] + v[3] * v[3]; }
;             ss += __builtin_bit_cast(float, __builtin_amdgcn_ds_swizzle(__builtin_bit_cast(int, ss), (1 << 10) | 0x1F)); ss += __builtin_bit_cast(float, __builtin_amdgcn_ds_swizzle(__builtin_bit_cast(int, ss), (2 << 10) | 0x1F));
;             ss += __builtin_bit_cast(float, __builtin_amdgcn_ds_swizzle(__builtin_bit_cast(int, ss), (4 << 10) | 0x1F));
;             const float rstd = __builtin_amdgcn_rsqf(ss * (1.0f / 256.0f) + EPSV);
;             bf16_t* mp = mix + (t0 + t) * DM + 1024 + h * 256 + 32 * g8;
; #pragma unroll
;             for (int x = 0; x < 4; ++x) {
;                 const u32x4 og = ogr[x];
;                 const f32x4 g0 = *(const LAS f32x4*)&gon[32 * g8 + 8 * x], g1 = *(const LAS f32x4*)&gon[32 * g8 + 8 * x + 4];
;                 const float gg2[8] = {g0[0], g0[1], g0[2], g0[3], g1[0], g1[1], g1[2], g1[3]};
;                 float res[8];
; #pragma unroll
;                 for (int y = 0; y < 4; ++y) { const float a0 = bf_lo(og[y]), a1 = bf_hi(og[y]);
;                     res[2 * y] = ov[8 * x + 2 * y] * rstd * gg2[2 * y] * a0;
;                     res[2 * y + 1] = ov[8 * x + 2 * y + 1] * rstd * gg2[2 * y + 1] * a1; }
;                 u32x4 wv4; wv4[0] = cvt_pk_bf16(res[0], res[1]); wv4[1] = cvt_pk_bf16(res[2], res[3]); wv4[2] = cvt_pk_bf16(res[4], res[5]); wv4[3] = cvt_pk_bf16(res[6], res[7]);
;                 *(u32x4*)(mp + 8 * x) = wv4;
;             }
	v_mfma_f32_32x32x16_bf16 v[0:15], v[68:71], v[64:67], v[0:15]
	ds_read_b128 v[64:67], v221
	ds_read_b128 v[68:71], v221 offset:16
	ds_read_b128 v[72:75], v221 offset:32
	ds_read_b128 v[76:79], v221 offset:48
	s_waitcnt lgkmcnt(3)
	v_mul_f32_e32 v80, v65, v65
	s_waitcnt lgkmcnt(2)
	v_mul_f32_e32 v81, v69, v69
	v_fmac_f32_e32 v80, v64, v64
	v_fmac_f32_e32 v81, v68, v68
	v_fmac_f32_e32 v80, v66, v66
	v_fmac_f32_e32 v81, v70, v70
	v_fmac_f32_e32 v80, v67, v67
	v_fmac_f32_e32 v81, v71, v71
	s_waitcnt lgkmcnt(1)
	v_mov_b32_e32 v82, v73
	s_waitcnt lgkmcnt(0)
	v_mov_b32_e32 v83, v77
	v_add_f32_e32 v84, v80, v81
	v_mov_b32_e32 v80, v72
	v_mov_b32_e32 v81, v76
	v_pk_mul_f32 v[82:83], v[82:83], v[82:83]
	s_nop 0
	v_pk_fma_f32 v[80:81], v[80:81], v[80:81], v[82:83]
	v_mov_b32_e32 v82, v74
	v_mov_b32_e32 v83, v78
	v_pk_fma_f32 v[80:81], v[82:83], v[82:83], v[80:81]
	v_mov_b32_e32 v82, v75
	v_mov_b32_e32 v83, v79
	v_pk_fma_f32 v[80:81], v[82:83], v[82:83], v[80:81]
	s_nop 0
	v_add_f32_e32 v80, v84, v80
	v_add_f32_e32 v92, v80, v81
	ds_read_b128 v[80:83], v221 offset:64
	ds_read_b128 v[84:87], v221 offset:80
	s_waitcnt lgkmcnt(1)
	v_mov_b32_e32 v90, v81
	s_waitcnt lgkmcnt(0)
	v_mov_b32_e32 v91, v85
	v_mov_b32_e32 v88, v80
	v_mov_b32_e32 v89, v84
	v_pk_mul_f32 v[90:91], v[90:91], v[90:91]
	s_nop 0
	v_pk_fma_f32 v[88:89], v[88:89], v[88:89], v[90:91]
	v_mov_b32_e32 v90, v82
	v_mov_b32_e32 v91, v86
	v_pk_fma_f32 v[88:89], v[90:91], v[90:91], v[88:89]
	v_mov_b32_e32 v90, v83
	v_mov_b32_e32 v91, v87
	v_pk_fma_f32 v[88:89], v[90:91], v[90:91], v[88:89]
	s_nop 0
	v_add_f32_e32 v88, v92, v88
	v_add_f32_e32 v227, v88, v89
	ds_read_b128 v[88:91], v221 offset:96
	ds_read_b128 v[92:95], v221 offset:112
	s_waitcnt lgkmcnt(1)
	v_mov_b32_e32 v228, v89
	s_waitcnt lgkmcnt(0)
	v_mov_b32_e32 v229, v93
	v_mov_b32_e32 v200, v88
	v_mov_b32_e32 v201, v92
	v_pk_mul_f32 v[228:229], v[228:229], v[228:229]
	s_nop 0
	v_pk_fma_f32 v[200:201], v[200:201], v[200:201], v[228:229]
	v_mov_b32_e32 v228, v90
	v_mov_b32_e32 v229, v94
	v_pk_fma_f32 v[200:201], v[228:229], v[228:229], v[200:201]
	v_mov_b32_e32 v228, v91
	v_mov_b32_e32 v229, v95
	v_pk_fma_f32 v[200:201], v[228:229], v[228:229], v[200:201]
	ds_read_b128 v[228:231], v208
	ds_read_b128 v[232:235], v208 offset:16
	ds_read_b128 v[236:239], v208 offset:32
	ds_read_b128 v[240:243], v208 offset:48
	v_add_f32_e32 v200, v227, v200
	v_add_f32_e32 v200, v200, v201
	ds_swizzle_b32 v201, v200 offset:swizzle(SWAP,1)
	s_waitcnt lgkmcnt(0)
	v_add_f32_e32 v200, v200, v201
	ds_swizzle_b32 v201, v200 offset:swizzle(SWAP,2)
	s_waitcnt lgkmcnt(0)
	v_add_f32_e32 v200, v200, v201
	ds_swizzle_b32 v201, v200 offset:swizzle(SWAP,4)
	s_waitcnt lgkmcnt(0)
	v_add_f32_e32 v200, v200, v201
	v_fmamk_f32 v200, v200, 0x3b800000, v181
	v_rsq_f32_e32 v244, v200
	v_lshl_add_u64 v[200:201], s[76:77], 0, v[188:189]
	v_pk_mul_f32 v[66:67], v[66:67], v[244:245] op_sel_hi:[1,0]
	s_nop 0
	v_pk_mul_f32 v[66:67], v[230:231], v[66:67]
	v_pk_mul_f32 v[68:69], v[68:69], v[244:245] op_sel_hi:[1,0]
	v_pk_mul_f32 v[64:65], v[64:65], v[244:245] op_sel_hi:[1,0]
	v_pk_mul_f32 v[66:67], v[66:67], v[176:177]
	v_lshlrev_b32_e32 v176, 16, v178
	v_and_b32_e32 v177, 0xffff0000, v178
	v_pk_mul_f32 v[68:69], v[232:233], v[68:69]
	v_pk_mul_f32 v[70:71], v[70:71], v[244:245] op_sel_hi:[1,0]
	v_pk_mul_f32 v[64:65], v[228:229], v[64:65]
	v_pk_mul_f32 v[68:69], v[68:69], v[176:177]
	v_lshlrev_b32_e32 v176, 16, v179
	v_and_b32_e32 v177, 0xffff0000, v179
	v_pk_mul_f32 v[70:71], v[234:235], v[70:71]
	v_pk_mul_f32 v[64:65], v[64:65], v[246:247]
	v_pk_mul_f32 v[70:71], v[70:71], v[176:177]
	v_add_co_u32_e32 v176, vcc, s33, v200
	v_cvt_pk_bf16_f32 v64, v64, v65
	v_cvt_pk_bf16_f32 v65, v66, v67
	v_cvt_pk_bf16_f32 v66, v68, v69
	v_cvt_pk_bf16_f32 v67, v70, v71
	v_addc_co_u32_e32 v177, vcc, 0, v201, vcc
	global_store_dwordx4 v[176:177], v[64:67], off offset:2048
	v_pk_mul_f32 v[68:69], v[74:75], v[244:245] op_sel_hi:[1,0]
	v_pk_mul_f32 v[70:71], v[76:77], v[244:245] op_sel_hi:[1,0]
	v_pk_mul_f32 v[66:67], v[72:73], v[244:245] op_sel_hi:[1,0]
	s_waitcnt vmcnt(9)
; #define LAS __attribute__((address_space(3)))
; __device__ __forceinline__ unsigned cvt_pk_bf16(float lo, float hi) { const bf16x2_t r = __builtin_convertvector((f32x2_t){lo, hi}, bf16x2_t); return __builtin_bit_cast(unsigned, r); }
; __device__ __forceinline__ float bf_lo(unsigned w) { return __uint_as_float(w << 16); }
; __device__ __forceinline__ float bf_hi(unsigned w) { return __uint_as_float(w & 0xffff0000u); }
; __device__ __forceinline__ void gla_unit(LAS unsigned char* lds, const unsigned char* ws, const float* g_onorm, const int b, const int h, const int wv) {
;     ...
;         __syncthreads();
; #pragma unroll
;         for (int i = 0; i < 2; ++i) { const int c = tid + 512 * i, row = c >> 4, cc = (c & 15) * 16;
;             *(LAS u32x4*)(lds + L_Q + row * QS + cc) = qr[par][i]; *(LAS u32x4*)(lds + L_K + row * QS + cc) = kr[par][i]; }
; #pragma unroll
;         for (int i = 0; i < 4; ++i) { const int c = tid + 512 * i; *(LAS u32x4*)(lds + L_V + (c >> 5) * VS + (c & 31) * 16) = vr[par][i]; }
;         if (tid < 32) {
;             const float L2E_ = 1.4426950408889634f;
;             *(LAS f32x4*)&dec[tid * 4] = (f32x4){__builtin_amdgcn_exp2f(dr[0] * L2E_), __builtin_amdgcn_exp2f(dr[1] * L2E_), __builtin_amdgcn_exp2f(dr[2] * L2E_), __builtin_amdgcn_exp2f(dr[3] * L2E_)};
;         }
;     ...
; #pragma unroll
;             for (int x = 0; x < 4; ++x) {
;                 const u32x4 og = ogr[x];
;                 const f32x4 g0 = *(const LAS f32x4*)&gon[32 * g8 + 8 * x], g1 = *(const LAS f32x4*)&gon[32 * g8 + 8 * x + 4];
;                 const float gg2[8] = {g0[0], g0[1], g0[2], g0[3], g1[0], g1[1], g1[2], g1[3]};
;                 float res[8];
; #pragma unroll
;                 for (int y = 0; y < 4; ++y) { const float a0 = bf_lo(og[y]), a1 = bf_hi(og[y]);
;                     res[2 * y] = ov[8 * x + 2 * y] * rstd * gg2[2 * y] * a0;
;                     res[2 * y + 1] = ov[8 * x + 2 * y + 1] * rstd * gg2[2 * y + 1] * a1; }
;                 u32x4 wv4; wv4[0] = cvt_pk_bf16(res[0], res[1]); wv4[1] = cvt_pk_bf16(res[2], res[3]); wv4[2] = cvt_pk_bf16(res[4], res[5]); wv4[3] = cvt_pk_bf16(res[6], res[7]);
;                 *(u32x4*)(mp + 8 * x) = wv4;
;             }
	v_lshlrev_b32_e32 v64, 16, v172
	v_and_b32_e32 v65, 0xffff0000, v172
	v_pk_mul_f32 v[66:67], v[236:237], v[66:67]
	v_pk_mul_f32 v[68:69], v[238:239], v[68:69]
	v_pk_mul_f32 v[64:65], v[66:67], v[64:65]
	v_lshlrev_b32_e32 v66, 16, v173
	v_and_b32_e32 v67, 0xffff0000, v173
	v_pk_mul_f32 v[66:67], v[68:69], v[66:67]
	v_lshlrev_b32_e32 v68, 16, v174
	v_and_b32_e32 v69, 0xffff0000, v174
	v_pk_mul_f32 v[70:71], v[240:241], v[70:71]
	v_pk_mul_f32 v[72:73], v[78:79], v[244:245] op_sel_hi:[1,0]
	v_pk_mul_f32 v[68:69], v[70:71], v[68:69]
	v_lshlrev_b32_e32 v70, 16, v175
	v_and_b32_e32 v71, 0xffff0000, v175
	v_pk_mul_f32 v[72:73], v[242:243], v[72:73]
	v_cvt_pk_bf16_f32 v64, v64, v65
	v_pk_mul_f32 v[70:71], v[72:73], v[70:71]
	v_cvt_pk_bf16_f32 v65, v66, v67
	v_cvt_pk_bf16_f32 v66, v68, v69
	v_cvt_pk_bf16_f32 v67, v70, v71
	global_store_dwordx4 v[176:177], v[64:67], off offset:2064
	ds_read_b128 v[64:67], v208 offset:64
	ds_read_b128 v[68:71], v208 offset:80
	v_pk_mul_f32 v[74:75], v[80:81], v[244:245] op_sel_hi:[1,0]
	v_lshlrev_b32_e32 v72, 16, v168
	v_and_b32_e32 v73, 0xffff0000, v168
	s_waitcnt lgkmcnt(1)
	v_pk_mul_f32 v[64:65], v[64:65], v[74:75]
	v_pk_mul_f32 v[74:75], v[82:83], v[244:245] op_sel_hi:[1,0]
	v_pk_mul_f32 v[64:65], v[64:65], v[72:73]
	v_lshlrev_b32_e32 v72, 16, v169
	v_and_b32_e32 v73, 0xffff0000, v169
	v_pk_mul_f32 v[66:67], v[66:67], v[74:75]
	v_pk_mul_f32 v[74:75], v[84:85], v[244:245] op_sel_hi:[1,0]
	v_pk_mul_f32 v[66:67], v[66:67], v[72:73]
	v_lshlrev_b32_e32 v72, 16, v170
	v_and_b32_e32 v73, 0xffff0000, v170
	s_waitcnt lgkmcnt(0)
	v_pk_mul_f32 v[68:69], v[68:69], v[74:75]
	v_pk_mul_f32 v[74:75], v[86:87], v[244:245] op_sel_hi:[1,0]
	v_pk_mul_f32 v[68:69], v[68:69], v[72:73]
	v_lshlrev_b32_e32 v72, 16, v171
	v_and_b32_e32 v73, 0xffff0000, v171
	v_pk_mul_f32 v[70:71], v[70:71], v[74:75]
	v_cvt_pk_bf16_f32 v64, v64, v65
	v_pk_mul_f32 v[70:71], v[70:71], v[72:73]
	v_cvt_pk_bf16_f32 v65, v66, v67
	v_cvt_pk_bf16_f32 v66, v68, v69
	v_cvt_pk_bf16_f32 v67, v70, v71
	global_store_dwordx4 v[176:177], v[64:67], off offset:2080
	ds_read_b128 v[64:67], v208 offset:96
	ds_read_b128 v[68:71], v208 offset:112
	v_pk_mul_f32 v[74:75], v[88:89], v[244:245] op_sel_hi:[1,0]
	v_lshlrev_b32_e32 v72, 16, v164
	v_and_b32_e32 v73, 0xffff0000, v164
	s_waitcnt lgkmcnt(1)
	v_pk_mul_f32 v[64:65], v[74:75], v[64:65]
	v_pk_mul_f32 v[74:75], v[90:91], v[244:245] op_sel_hi:[1,0]
	v_pk_mul_f32 v[64:65], v[64:65], v[72:73]
	v_lshlrev_b32_e32 v72, 16, v165
	v_and_b32_e32 v73, 0xffff0000, v165
	v_pk_mul_f32 v[66:67], v[74:75], v[66:67]
	v_pk_mul_f32 v[74:75], v[92:93], v[244:245] op_sel_hi:[1,0]
	v_pk_mul_f32 v[66:67], v[66:67], v[72:73]
	v_lshlrev_b32_e32 v72, 16, v166
	v_and_b32_e32 v73, 0xffff0000, v166
	s_waitcnt lgkmcnt(0)
	v_pk_mul_f32 v[68:69], v[74:75], v[68:69]
	v_pk_mul_f32 v[74:75], v[94:95], v[244:245] op_sel_hi:[1,0]
	v_pk_mul_f32 v[68:69], v[68:69], v[72:73]
	v_lshlrev_b32_e32 v72, 16, v167
	v_and_b32_e32 v73, 0xffff0000, v167
	v_pk_mul_f32 v[70:71], v[74:75], v[70:71]
	v_cvt_pk_bf16_f32 v64, v64, v65
	v_pk_mul_f32 v[70:71], v[70:71], v[72:73]
	v_cvt_pk_bf16_f32 v65, v66, v67
	v_cvt_pk_bf16_f32 v66, v68, v69
	v_cvt_pk_bf16_f32 v67, v70, v71
	global_store_dwordx4 v[176:177], v[64:67], off offset:2096
	s_barrier
	s_waitcnt vmcnt(20)
	ds_write_b128 v209, v[132:135]
	ds_write_b128 v209, v[136:139] offset:17408
	ds_write_b128 v210, v[140:143]
	ds_write_b128 v210, v[144:147] offset:17408
	ds_write_b128 v211, v[148:151]
	ds_write_b128 v212, v[152:155]
	ds_write_b128 v213, v[156:159]
	ds_write_b128 v214, v[160:163]
	s_and_saveexec_b64 s[42:43], s[0:1]
	s_cbranch_execz .LBB0_648
	s_waitcnt vmcnt(12)
	v_mul_f32_e32 v64, 0x3fb8aa3b, v124
	v_mul_f32_e32 v65, 0x3fb8aa3b, v125
	v_mul_f32_e32 v66, 0x3fb8aa3b, v126
	v_mul_f32_e32 v67, 0x3fb8aa3b, v127
	v_exp_f32_e32 v64, v64
	v_exp_f32_e32 v65, v65
	v_exp_f32_e32 v66, v66
	v_exp_f32_e32 v67, v67
	ds_write_b128 v226, v[64:67]

; #define LAS __attribute__((address_space(3)))
; __device__ __forceinline__ void gla_unit(LAS unsigned char* lds, const unsigned char* ws, const float* g_onorm, const int b, const int h, const int wv) {
;     ...
;         f32x16 O[2];
; #pragma unroll
;         for (int tt = 0; tt < 2; ++tt)
; #pragma unroll
;             for (int r = 0; r < 16; ++r) O[tt][r] = 0.f;
; #pragma unroll
;         for (int et = 0; et < 4; ++et)
; #pragma unroll
;             for (int s2 = 0; s2 < 2; ++s2) {
;                 const bf16x8 sb = pack8(S[et], s2);
; #pragma unroll
;                 for (int tt = 0; tt < 2; ++tt) {
;                     const bf16x8 aq = ld2x64(qb8 + 32 * tt * QS + (32 * et + 16 * s2) * 2);
;                     O[tt] = __builtin_amdgcn_mfma_f32_32x32x16_bf16(aq, sb, O[tt], 0, 0, 0);
;                 }
;             }
;         __syncthreads();
; #pragma unroll
;         for (int pr = 0; pr < 3; ++pr) {
;             const int st = (pr == 2) ? 1 : 0, tt = (pr == 0) ? 0 : 1;
; #pragma unroll
;             for (int s2 = 0; s2 < 2; ++s2) {
;                 const bf16x8 ax = *(const LAS bf16x8*)(frb + (pr * 2 + s2) * 1024);
;                 const LAS unsigned char* vp = vP + (32 * st + 16 * s2) * VS;
;                 const bf16x8 bv = tr8(vp, vp + 8 * VS);
;                 O[tt] = __builtin_amdgcn_mfma_f32_32x32x16_bf16(ax, bv, O[tt], 0, 0, 0);
;             }
;         }
;         __builtin_amdgcn_sched_barrier(0);
; #pragma unroll
;         for (int tt = 0; tt < 2; ++tt)
; #pragma unroll
;             for (int r = 0; r < 16; ++r) ob[(32 * tt + (r & 3) + 8 * (r >> 2)) * OS] = O[tt][r];
.LBB0_1692:
	ds_read2_b64 v[64:67], v222 offset1:2
	v_cvt_pk_bf16_f32 v68, v48, v49
	v_cvt_pk_bf16_f32 v69, v50, v51
	v_cvt_pk_bf16_f32 v70, v52, v53
	v_cvt_pk_bf16_f32 v71, v54, v55
	ds_read2_b64 v[192:195], v222 offset0:4 offset1:6
	v_cvt_pk_bf16_f32 v198, v56, v57
	v_cvt_pk_bf16_f32 v199, v58, v59
	v_cvt_pk_bf16_f32 v200, v60, v61
	s_waitcnt lgkmcnt(1)
	v_mfma_f32_32x32x16_bf16 v[80:95], v[64:67], v[68:71], 0
	ds_read2_b64 v[64:67], v223 offset0:64 offset1:66
	v_cvt_pk_bf16_f32 v201, v62, v63
	s_waitcnt lgkmcnt(1)
	s_nop 0
	v_mfma_f32_32x32x16_bf16 v[80:95], v[192:195], v[198:201], v[80:95]
	ds_read2_b64 v[192:195], v223 offset0:68 offset1:70
	s_waitcnt lgkmcnt(1)
	v_mfma_f32_32x32x16_bf16 v[64:79], v[64:67], v[68:71], 0
	s_waitcnt lgkmcnt(0)
	v_mfma_f32_32x32x16_bf16 v[64:79], v[192:195], v[198:201], v[64:79]
	ds_read2_b64 v[192:195], v222 offset0:8 offset1:10
	ds_read2_b64 v[224:227], v223 offset0:72 offset1:74
	ds_read2_b64 v[232:235], v222 offset0:12 offset1:14
	v_cvt_pk_bf16_f32 v198, v16, v17
	v_cvt_pk_bf16_f32 v199, v18, v19
	v_cvt_pk_bf16_f32 v200, v20, v21
	v_cvt_pk_bf16_f32 v201, v22, v23
	s_waitcnt lgkmcnt(2)
	s_nop 0
	v_mfma_f32_32x32x16_bf16 v[80:95], v[192:195], v[198:201], v[80:95]
	ds_read2_b64 v[236:239], v223 offset0:76 offset1:78
	s_waitcnt lgkmcnt(2)
	v_mfma_f32_32x32x16_bf16 v[64:79], v[224:227], v[198:201], v[64:79]
	ds_read2_b64 v[192:195], v222 offset0:16 offset1:18
	v_cvt_pk_bf16_f32 v198, v24, v25
	v_cvt_pk_bf16_f32 v199, v26, v27
	v_cvt_pk_bf16_f32 v200, v28, v29
	v_cvt_pk_bf16_f32 v201, v30, v31
	s_waitcnt lgkmcnt(2)
	s_nop 0
	v_mfma_f32_32x32x16_bf16 v[80:95], v[232:235], v[198:201], v[80:95]
	ds_read2_b64 v[224:227], v223 offset0:80 offset1:82
	s_waitcnt lgkmcnt(2)
	v_mfma_f32_32x32x16_bf16 v[64:79], v[236:239], v[198:201], v[64:79]
	ds_read2_b64 v[232:235], v222 offset0:20 offset1:22
	v_cvt_pk_bf16_f32 v198, v32, v33
	v_cvt_pk_bf16_f32 v199, v34, v35
	v_cvt_pk_bf16_f32 v200, v36, v37
	v_cvt_pk_bf16_f32 v201, v38, v39
	s_waitcnt lgkmcnt(2)
	s_nop 0
	v_mfma_f32_32x32x16_bf16 v[80:95], v[192:195], v[198:201], v[80:95]
	ds_read2_b64 v[236:239], v223 offset0:84 offset1:86
	s_waitcnt lgkmcnt(2)
	v_mfma_f32_32x32x16_bf16 v[64:79], v[224:227], v[198:201], v[64:79]
	ds_read2_b64 v[192:195], v222 offset0:24 offset1:26
	v_cvt_pk_bf16_f32 v198, v40, v41
	v_cvt_pk_bf16_f32 v199, v42, v43
	v_cvt_pk_bf16_f32 v200, v44, v45
	v_cvt_pk_bf16_f32 v201, v46, v47
	s_waitcnt lgkmcnt(2)
	s_nop 0
	v_mfma_f32_32x32x16_bf16 v[80:95], v[232:235], v[198:201], v[80:95]
	ds_read2_b64 v[224:227], v223 offset0:88 offset1:90
	s_waitcnt lgkmcnt(2)
	v_mfma_f32_32x32x16_bf16 v[64:79], v[236:239], v[198:201], v[64:79]
	ds_read2_b64 v[232:235], v222 offset0:28 offset1:30
	v_cvt_pk_bf16_f32 v198, v0, v1
	v_cvt_pk_bf16_f32 v199, v2, v3
	v_cvt_pk_bf16_f32 v200, v4, v5
	v_cvt_pk_bf16_f32 v201, v6, v7
	s_waitcnt lgkmcnt(2)
	s_nop 0
	v_mfma_f32_32x32x16_bf16 v[80:95], v[192:195], v[198:201], v[80:95]
	ds_read2_b64 v[236:239], v223 offset0:92 offset1:94
	s_waitcnt lgkmcnt(2)
	v_mfma_f32_32x32x16_bf16 v[64:79], v[224:227], v[198:201], v[64:79]
	v_cvt_pk_bf16_f32 v198, v8, v9
	v_cvt_pk_bf16_f32 v199, v10, v11
	v_cvt_pk_bf16_f32 v200, v12, v13
	v_cvt_pk_bf16_f32 v201, v14, v15
	s_waitcnt lgkmcnt(1)
	s_nop 0
	v_mfma_f32_32x32x16_bf16 v[80:95], v[232:235], v[198:201], v[80:95]
	s_waitcnt lgkmcnt(0)
	s_barrier
	v_mfma_f32_32x32x16_bf16 v[64:79], v[236:239], v[198:201], v[64:79]
	ds_read_b128 v[192:195], v206
	ds_read_b64_tr_b16 v[198:199], v218
	ds_read_b64_tr_b16 v[200:201], v218 offset:4608
	ds_read_b128 v[222:225], v206 offset:1024
	ds_read_b64_tr_b16 v[226:227], v218 offset:9216
	ds_read_b64_tr_b16 v[228:229], v218 offset:13824
	s_waitcnt lgkmcnt(3)
	v_mfma_f32_32x32x16_bf16 v[80:95], v[192:195], v[198:201], v[80:95]
	s_waitcnt lgkmcnt(0)
	v_mfma_f32_32x32x16_bf16 v[80:95], v[222:225], v[226:229], v[80:95]
	ds_read_b128 v[192:195], v206 offset:2048
	ds_read_b128 v[222:225], v206 offset:3072
	s_waitcnt lgkmcnt(1)
	v_mfma_f32_32x32x16_bf16 v[64:79], v[192:195], v[198:201], v[64:79]
	s_waitcnt lgkmcnt(0)
	v_mfma_f32_32x32x16_bf16 v[64:79], v[222:225], v[226:229], v[64:79]
	ds_read_b128 v[192:195], v206 offset:4096
	ds_read_b64_tr_b16 v[198:199], v218 offset:18432
	ds_read_b64_tr_b16 v[200:201], v218 offset:23040
	ds_read_b128 v[222:225], v206 offset:5120
	ds_read_b64_tr_b16 v[226:227], v218 offset:27648
	ds_read_b64_tr_b16 v[228:229], v218 offset:32256
	s_waitcnt lgkmcnt(3)
	v_mfma_f32_32x32x16_bf16 v[64:79], v[192:195], v[198:201], v[64:79]
	s_waitcnt lgkmcnt(0)
	v_mfma_f32_32x32x16_bf16 v[64:79], v[222:225], v[226:229], v[64:79]
	ds_write_b32 v207, v80
	ds_write_b32 v207, v81 offset:1040
	ds_write_b32 v207, v82 offset:2080
	ds_write_b32 v207, v83 offset:3120
	ds_write_b32 v207, v84 offset:8320
	ds_write_b32 v207, v85 offset:9360
	ds_write_b32 v207, v86 offset:10400
	ds_write_b32 v207, v87 offset:11440
	ds_write_b32 v207, v88 offset:16640
	ds_write_b32 v207, v89 offset:17680
	ds_write_b32 v207, v90 offset:18720
	ds_write_b32 v207, v91 offset:19760
	ds_write_b32 v207, v92 offset:24960
	ds_write_b32 v207, v93 offset:26000
	ds_write_b32 v207, v94 offset:27040
	ds_write_b32 v207, v95 offset:28080
	ds_write_b32 v207, v64 offset:33280
	ds_write_b32 v207, v65 offset:34320
	ds_write_b32 v207, v66 offset:35360
	ds_write_b32 v207, v67 offset:36400
	ds_write_b32 v207, v68 offset:41600
	ds_write_b32 v207, v69 offset:42640
	ds_write_b32 v207, v70 offset:43680
	ds_write_b32 v207, v71 offset:44720
	ds_write_b32 v207, v72 offset:49920
	ds_write_b32 v207, v73 offset:50960
	ds_write_b32 v207, v74 offset:52000
	ds_write_b32 v207, v75 offset:53040
	ds_write_b32 v207, v76 offset:58240
	ds_write_b32 v207, v77 offset:59280
	ds_write_b32 v207, v78 offset:60320
	ds_write_b32 v207, v79 offset:61360
	ds_read_b128 v[64:67], v205 offset:96
	ds_read_b128 v[68:71], v205 offset:64
	ds_read_b128 v[72:75], v205 offset:32
	ds_read_b128 v[76:79], v205
	s_waitcnt vmcnt(11)
; #define LAS __attribute__((address_space(3)))
; __device__ __forceinline__ void gla_unit(LAS unsigned char* lds, const unsigned char* ws, const float* g_onorm, const int b, const int h, const int wv) {
;     ...
; #pragma unroll
;         for (int et = 0; et < 4; ++et)
; #pragma unroll
;             for (int rg = 0; rg < 4; ++rg) { const f32x4 dl = *(const LAS f32x4*)&decb[32 * et + 8 * rg];
; #pragma unroll
;                 for (int x = 0; x < 4; ++x) S[et][4 * rg + x] *= dl[x]; }
; #pragma unroll
;         for (int ks = 0; ks < 4; ++ks) {
;             const LAS unsigned char* vp = vN + 16 * ks * VS;
;             const bf16x8 bv = tr8(vp, vp + 4 * VS);
; #pragma unroll
;             for (int et = 0; et < 4; ++et) {
;                 const LAS unsigned char* kp = keN + 32 * et * 2 + 16 * ks * ES;
;                 const bf16x8 ak = tr8(kp, kp + 4 * ES);
;                 S[et] = __builtin_amdgcn_mfma_f32_32x32x16_bf16(ak, bv, S[et], 0, 0, 0);
;             }
;         }
	v_lshlrev_b32_e32 v232, 16, v176
	s_waitcnt lgkmcnt(3)
	v_pk_mul_f32 v[62:63], v[62:63], v[66:67]
	s_waitcnt lgkmcnt(2)
	v_pk_mul_f32 v[58:59], v[58:59], v[70:71]
	v_pk_mul_f32 v[60:61], v[60:61], v[64:65]
	s_waitcnt lgkmcnt(0)
	v_pk_mul_f32 v[50:51], v[50:51], v[78:79]
	v_pk_mul_f32 v[56:57], v[56:57], v[68:69]
	ds_read_b128 v[64:67], v205 offset:192
	ds_read_b128 v[68:71], v205 offset:224
	ds_read_b128 v[78:81], v205 offset:128
	ds_read_b128 v[82:85], v205 offset:160
	v_pk_mul_f32 v[54:55], v[54:55], v[74:75]
	v_pk_mul_f32 v[52:53], v[52:53], v[72:73]
	v_pk_mul_f32 v[48:49], v[48:49], v[76:77]
	s_waitcnt lgkmcnt(2)
	v_pk_mul_f32 v[30:31], v[30:31], v[70:71]
	v_pk_mul_f32 v[26:27], v[26:27], v[66:67]
	s_waitcnt lgkmcnt(0)
	v_pk_mul_f32 v[22:23], v[22:23], v[84:85]
	v_pk_mul_f32 v[18:19], v[18:19], v[80:81]
	v_pk_mul_f32 v[28:29], v[28:29], v[68:69]
	v_pk_mul_f32 v[24:25], v[24:25], v[64:65]
	v_pk_mul_f32 v[20:21], v[20:21], v[82:83]
	ds_read_b128 v[64:67], v205 offset:256
	ds_read_b128 v[68:71], v205 offset:288
	ds_read_b128 v[72:75], v205 offset:320
	ds_read_b128 v[80:83], v205 offset:352
	ds_read_b64_tr_b16 v[84:85], v219
	ds_read_b64_tr_b16 v[86:87], v219 offset:2304
	ds_read_b64_tr_b16 v[90:91], v220 offset:1280
	ds_read_b64_tr_b16 v[88:89], v220
	ds_read_b64_tr_b16 v[92:93], v220 offset:64
	ds_read_b64_tr_b16 v[192:193], v220 offset:128
	ds_read_b64_tr_b16 v[198:199], v220 offset:192
	ds_read_b64_tr_b16 v[94:95], v220 offset:1344
	ds_read_b64_tr_b16 v[194:195], v220 offset:1408
	ds_read_b64_tr_b16 v[200:201], v220 offset:1472
	ds_read_b64_tr_b16 v[222:223], v219 offset:9216
	ds_read_b64_tr_b16 v[224:225], v219 offset:11520
	s_waitcnt lgkmcnt(8)
	v_mfma_f32_32x32x16_bf16 v[48:63], v[88:91], v[84:87], v[48:63]
	v_mul_f32_e64 v16, v16, v78
	v_mul_f32_e64 v17, v17, v79
	v_mul_f32_e64 v42, v42, v74
	v_mul_f32_e64 v43, v43, v75
	v_mul_f32_e64 v38, v38, v70
	v_mul_f32_e64 v39, v39, v71
	v_pk_mul_f32 v[34:35], v[34:35], v[66:67]
	v_pk_mul_f32 v[44:45], v[44:45], v[80:81]
	v_pk_mul_f32 v[40:41], v[40:41], v[72:73]
	ds_read_b128 v[70:73], v205 offset:448
	ds_read_b128 v[74:77], v205 offset:480
	v_pk_mul_f32 v[36:37], v[36:37], v[68:69]
	ds_read_b128 v[66:69], v205 offset:384
	ds_read_b128 v[78:81], v205 offset:416
	v_pk_mul_f32 v[46:47], v[46:47], v[82:83]
	v_pk_mul_f32 v[32:33], v[32:33], v[64:65]
	s_waitcnt lgkmcnt(2)
	v_pk_mul_f32 v[14:15], v[14:15], v[76:77]
	v_pk_mul_f32 v[10:11], v[10:11], v[72:73]
	s_waitcnt lgkmcnt(0)
	v_pk_mul_f32 v[6:7], v[6:7], v[80:81]
	v_pk_mul_f32 v[2:3], v[2:3], v[68:69]
	v_pk_mul_f32 v[12:13], v[12:13], v[74:75]
	v_pk_mul_f32 v[8:9], v[8:9], v[70:71]
	v_pk_mul_f32 v[4:5], v[4:5], v[78:79]
	v_pk_mul_f32 v[0:1], v[0:1], v[66:67]
	v_mfma_f32_32x32x16_bf16 v[16:31], v[92:95], v[84:87], v[16:31]
	ds_read_b64_tr_b16 v[66:67], v220 offset:6400
	ds_read_b64_tr_b16 v[64:65], v220 offset:5120
	ds_read_b64_tr_b16 v[68:69], v220 offset:5184
	ds_read_b64_tr_b16 v[72:73], v220 offset:5248
	ds_read_b64_tr_b16 v[76:77], v220 offset:5312
	ds_read_b64_tr_b16 v[70:71], v220 offset:6464
	ds_read_b64_tr_b16 v[74:75], v220 offset:6528
	ds_read_b64_tr_b16 v[78:79], v220 offset:6592
	v_and_b32_e32 v233, 0xffff0000, v176
	s_add_i32 s66, s66, 2
	v_lshl_add_u64 v[182:183], v[182:183], 0, s[60:61]
	v_lshl_add_u64 v[184:185], v[184:185], 0, s[62:63]
	v_lshl_add_u64 v[186:187], v[186:187], 0, s[64:65]
	v_lshl_add_u64 v[188:189], v[188:189], 0, s[68:69]
	v_mfma_f32_32x32x16_bf16 v[32:47], v[192:195], v[84:87], v[32:47]
	s_cmp_lt_u32 s73, 30
	v_lshl_add_u64 v[190:191], v[190:191], 0, s[62:63]
	v_mfma_f32_32x32x16_bf16 v[0:15], v[198:201], v[84:87], v[0:15]
	s_waitcnt lgkmcnt(6)
	v_mfma_f32_32x32x16_bf16 v[48:63], v[64:67], v[222:225], v[48:63]
	s_waitcnt lgkmcnt(2)
	v_mfma_f32_32x32x16_bf16 v[16:31], v[68:71], v[222:225], v[16:31]
	s_waitcnt lgkmcnt(1)
	v_mfma_f32_32x32x16_bf16 v[32:47], v[72:75], v[222:225], v[32:47]
	s_waitcnt lgkmcnt(0)
	v_mfma_f32_32x32x16_bf16 v[0:15], v[76:79], v[222:225], v[0:15]
	ds_read_b64_tr_b16 v[64:65], v219 offset:18432
	ds_read_b64_tr_b16 v[66:67], v219 offset:20736
	ds_read_b64_tr_b16 v[70:71], v220 offset:11520
	ds_read_b64_tr_b16 v[68:69], v220 offset:10240
	ds_read_b64_tr_b16 v[72:73], v220 offset:10304
	ds_read_b64_tr_b16 v[76:77], v220 offset:10368
	ds_read_b64_tr_b16 v[80:81], v220 offset:10432
	ds_read_b64_tr_b16 v[74:75], v220 offset:11584
	ds_read_b64_tr_b16 v[78:79], v220 offset:11648
	ds_read_b64_tr_b16 v[82:83], v220 offset:11712
	ds_read_b64_tr_b16 v[84:85], v219 offset:27648
	ds_read_b64_tr_b16 v[86:87], v219 offset:29952
	s_waitcnt lgkmcnt(8)
	v_mfma_f32_32x32x16_bf16 v[48:63], v[68:71], v[64:67], v[48:63]
	ds_read_b64_tr_b16 v[68:69], v220 offset:16640
	s_waitcnt lgkmcnt(5)
	v_mfma_f32_32x32x16_bf16 v[16:31], v[72:75], v[64:67], v[16:31]
	s_waitcnt lgkmcnt(4)
	v_mfma_f32_32x32x16_bf16 v[32:47], v[76:79], v[64:67], v[32:47]
	s_waitcnt lgkmcnt(3)
	v_mfma_f32_32x32x16_bf16 v[0:15], v[80:83], v[64:67], v[0:15]
	ds_read_b64_tr_b16 v[66:67], v220 offset:15360
	ds_read_b64_tr_b16 v[70:71], v220 offset:15424
	ds_read_b64_tr_b16 v[74:75], v220 offset:15488
	ds_read_b64_tr_b16 v[78:79], v220 offset:15552
	ds_read_b64_tr_b16 v[72:73], v220 offset:16704
	ds_read_b64_tr_b16 v[76:77], v220 offset:16768
	ds_read_b64_tr_b16 v[80:81], v220 offset:16832
	s_waitcnt lgkmcnt(0)
	s_barrier
; #define LAS __attribute__((address_space(3)))
; __device__ __forceinline__ unsigned cvt_pk_bf16(float lo, float hi) { const bf16x2_t r = __builtin_convertvector((f32x2_t){lo, hi}, bf16x2_t); return __builtin_bit_cast(unsigned, r); }
; __device__ __forceinline__ void gla_unit(LAS unsigned char* lds, const unsigned char* ws, const float* g_onorm, const int b, const int h, const int wv) {
;     ...
;                 S[et] = __builtin_amdgcn_mfma_f32_32x32x16_bf16(ak, bv, S[et], 0, 0, 0);
;             }
;         }
;         __syncthreads();
;         {
;             const int t = tid >> 3, g8 = tid & 7;
;             float ov[32]; float ss = 0.f;
; #pragma unroll
;             for (int x = 0; x < 8; ++x) { const f32x4 v = *(const LAS f32x4*)&obuf[t * OS + 32 * g8 + 4 * x]; ov[4 * x] = v[0]; ov[4 * x + 1] = v[1]; ov[4 * x + 2] = v[2]; ov[4 * x + 3] = v[3];
;                 ss += v[0] * v[0] + v[1] * v[1] + v[2] * v[2] + v[3] * v[3]; }
;             ss += __builtin_bit_cast(float, __builtin_amdgcn_ds_swizzle(__builtin_bit_cast(int, ss), (1 << 10) | 0x1F)); ss += __builtin_bit_cast(float, __builtin_amdgcn_ds_swizzle(__builtin_bit_cast(int, ss), (2 << 10) | 0x1F));
;             ss += __builtin_bit_cast(float, __builtin_amdgcn_ds_swizzle(__builtin_bit_cast(int, ss), (4 << 10) | 0x1F));
;             const float rstd = __builtin_amdgcn_rsqf(ss * (1.0f / 256.0f) + EPSV);
;             bf16_t* mp = mix + (t0 + t) * DM + 1024 + h * 256 + 32 * g8;
; #pragma unroll
;             for (int x = 0; x < 4; ++x) {
;                 const u32x4 og = ogr[x];
;                 const f32x4 g0 = *(const LAS f32x4*)&gon[32 * g8 + 8 * x], g1 = *(const LAS f32x4*)&gon[32 * g8 + 8 * x + 4];
;                 const float gg2[8] = {g0[0], g0[1], g0[2], g0[3], g1[0], g1[1], g1[2], g1[3]};
;                 float res[8];
; #pragma unroll
;                 for (int y = 0; y < 4; ++y) { const float a0 = bf_lo(og[y]), a1 = bf_hi(og[y]);
;                     res[2 * y] = ov[8 * x + 2 * y] * rstd * gg2[2 * y] * a0;
;                     res[2 * y + 1] = ov[8 * x + 2 * y + 1] * rstd * gg2[2 * y + 1] * a1; }
;                 u32x4 wv4; wv4[0] = cvt_pk_bf16(res[0], res[1]); wv4[1] = cvt_pk_bf16(res[2], res[3]); wv4[2] = cvt_pk_bf16(res[4], res[5]); wv4[3] = cvt_pk_bf16(res[6], res[7]);
;                 *(u32x4*)(mp + 8 * x) = wv4;
;             }
	v_mfma_f32_32x32x16_bf16 v[48:63], v[66:69], v[84:87], v[48:63]
	ds_read_b128 v[64:67], v221
	ds_read_b128 v[88:91], v221 offset:16
	ds_read_b128 v[92:95], v221 offset:32
	ds_read_b128 v[192:195], v221 offset:48
	s_waitcnt lgkmcnt(3)
	v_mul_f32_e32 v68, v65, v65
	s_waitcnt lgkmcnt(2)
	v_mul_f32_e32 v69, v89, v89
	v_fmac_f32_e32 v68, v64, v64
	v_fmac_f32_e32 v69, v88, v88
	v_fmac_f32_e32 v68, v66, v66
	v_fmac_f32_e32 v69, v90, v90
	v_mfma_f32_32x32x16_bf16 v[16:31], v[70:73], v[84:87], v[16:31]
	v_fmac_f32_e32 v68, v67, v67
	v_fmac_f32_e32 v69, v91, v91
	s_waitcnt lgkmcnt(1)
	v_mov_b32_e32 v70, v93
	s_waitcnt lgkmcnt(0)
	v_mov_b32_e32 v71, v193
	v_add_f32_e32 v222, v68, v69
	v_mov_b32_e32 v68, v92
	v_mov_b32_e32 v69, v192
	v_pk_mul_f32 v[70:71], v[70:71], v[70:71]
	v_mov_b32_e32 v82, v95
	v_pk_fma_f32 v[68:69], v[68:69], v[68:69], v[70:71]
	v_mov_b32_e32 v70, v94
	v_mov_b32_e32 v71, v194
	v_pk_fma_f32 v[72:73], v[70:71], v[70:71], v[68:69]
	ds_read_b128 v[68:71], v221 offset:64
	ds_read_b128 v[198:201], v221 offset:80
	v_mov_b32_e32 v83, v195
	v_pk_fma_f32 v[72:73], v[82:83], v[82:83], v[72:73]
	v_mfma_f32_32x32x16_bf16 v[32:47], v[74:77], v[84:87], v[32:47]
	v_add_f32_e32 v72, v222, v72
	s_waitcnt lgkmcnt(1)
	v_mov_b32_e32 v82, v69
	s_waitcnt lgkmcnt(0)
	v_mov_b32_e32 v83, v199
	ds_read_b128 v[222:225], v221 offset:96
	ds_read_b128 v[226:229], v221 offset:112
	v_add_f32_e32 v230, v72, v73
	v_mov_b32_e32 v72, v68
	v_mov_b32_e32 v73, v198
	v_pk_mul_f32 v[82:83], v[82:83], v[82:83]
	v_mfma_f32_32x32x16_bf16 v[0:15], v[78:81], v[84:87], v[0:15]
	v_fma_f32 v72, v72, v72, v82
	v_fma_f32 v73, v73, v73, v83
	v_mov_b32_e32 v82, v70
	v_mov_b32_e32 v83, v200
	v_fma_f32 v72, v82, v82, v72
	v_fma_f32 v73, v83, v83, v73
	v_mov_b32_e32 v82, v71
	v_mov_b32_e32 v83, v201
	v_pk_fma_f32 v[72:73], v[82:83], v[82:83], v[72:73]
	s_waitcnt lgkmcnt(1)
	v_mov_b32_e32 v82, v223
	v_add_f32_e32 v72, v230, v72
	s_waitcnt lgkmcnt(0)
	v_mov_b32_e32 v83, v227
	v_add_f32_e32 v230, v72, v73
	v_mov_b32_e32 v72, v222
	v_mov_b32_e32 v73, v226
	v_pk_mul_f32 v[82:83], v[82:83], v[82:83]
	s_nop 0
	v_pk_fma_f32 v[72:73], v[72:73], v[72:73], v[82:83]
	v_mov_b32_e32 v82, v224
	v_mov_b32_e32 v83, v228
	v_pk_fma_f32 v[72:73], v[82:83], v[82:83], v[72:73]
	v_mov_b32_e32 v82, v225
	v_mov_b32_e32 v83, v229
	v_pk_fma_f32 v[72:73], v[82:83], v[82:83], v[72:73]
	s_nop 0
	v_add_f32_e32 v72, v230, v72
	v_add_f32_e32 v72, v72, v73
	ds_swizzle_b32 v73, v72 offset:swizzle(SWAP,1)
	s_waitcnt lgkmcnt(0)
	v_add_f32_e32 v72, v72, v73
	ds_swizzle_b32 v73, v72 offset:swizzle(SWAP,2)
	s_waitcnt lgkmcnt(0)
	v_add_f32_e32 v72, v72, v73
	ds_swizzle_b32 v73, v72 offset:swizzle(SWAP,4)
	s_waitcnt lgkmcnt(0)
	v_add_f32_e32 v72, v72, v73
	v_fmamk_f32 v72, v72, 0x3b800000, v181
	v_rsq_f32_e32 v230, v72
	ds_read_b128 v[72:75], v208
	ds_read_b128 v[76:79], v208 offset:16
	ds_read_b128 v[80:83], v208 offset:32
	ds_read_b128 v[84:87], v208 offset:48
	v_pk_mul_f32 v[64:65], v[64:65], v[230:231] op_sel_hi:[1,0]
	v_pk_mul_f32 v[66:67], v[66:67], v[230:231] op_sel_hi:[1,0]
	s_waitcnt lgkmcnt(3)
	v_pk_mul_f32 v[64:65], v[72:73], v[64:65]
	v_lshlrev_b32_e32 v72, 16, v177
	v_and_b32_e32 v73, 0xffff0000, v177
	v_pk_mul_f32 v[66:67], v[74:75], v[66:67]
	v_pk_mul_f32 v[74:75], v[88:89], v[230:231] op_sel_hi:[1,0]
	v_pk_mul_f32 v[66:67], v[66:67], v[72:73]
	v_lshlrev_b32_e32 v72, 16, v178
	v_and_b32_e32 v73, 0xffff0000, v178
	s_waitcnt lgkmcnt(2)
; #define LAS __attribute__((address_space(3)))
; __device__ __forceinline__ unsigned cvt_pk_bf16(float lo, float hi) { const bf16x2_t r = __builtin_convertvector((f32x2_t){lo, hi}, bf16x2_t); return __builtin_bit_cast(unsigned, r); }
; __device__ __forceinline__ float bf_lo(unsigned w) { return __uint_as_float(w << 16); }
; __device__ __forceinline__ float bf_hi(unsigned w) { return __uint_as_float(w & 0xffff0000u); }
; __device__ __forceinline__ void gla_unit(LAS unsigned char* lds, const unsigned char* ws, const float* g_onorm, const int b, const int h, const int wv) {
;     ...
;             bf16_t* mp = mix + (t0 + t) * DM + 1024 + h * 256 + 32 * g8;
; #pragma unroll
;             for (int x = 0; x < 4; ++x) {
;                 const u32x4 og = ogr[x];
;                 const f32x4 g0 = *(const LAS f32x4*)&gon[32 * g8 + 8 * x], g1 = *(const LAS f32x4*)&gon[32 * g8 + 8 * x + 4];
;                 const float gg2[8] = {g0[0], g0[1], g0[2], g0[3], g1[0], g1[1], g1[2], g1[3]};
;                 float res[8];
; #pragma unroll
;                 for (int y = 0; y < 4; ++y) { const float a0 = bf_lo(og[y]), a1 = bf_hi(og[y]);
;                     res[2 * y] = ov[8 * x + 2 * y] * rstd * gg2[2 * y] * a0;
;                     res[2 * y + 1] = ov[8 * x + 2 * y + 1] * rstd * gg2[2 * y + 1] * a1; }
;                 u32x4 wv4; wv4[0] = cvt_pk_bf16(res[0], res[1]); wv4[1] = cvt_pk_bf16(res[2], res[3]); wv4[2] = cvt_pk_bf16(res[4], res[5]); wv4[3] = cvt_pk_bf16(res[6], res[7]);
;                 *(u32x4*)(mp + 8 * x) = wv4;
;             }
	v_pk_mul_f32 v[74:75], v[76:77], v[74:75]
	v_pk_mul_f32 v[76:77], v[90:91], v[230:231] op_sel_hi:[1,0]
	v_pk_mul_f32 v[72:73], v[74:75], v[72:73]
	v_lshlrev_b32_e32 v74, 16, v179
	v_and_b32_e32 v75, 0xffff0000, v179
	v_pk_mul_f32 v[76:77], v[78:79], v[76:77]
	v_pk_mul_f32 v[64:65], v[64:65], v[232:233]
	v_pk_mul_f32 v[74:75], v[76:77], v[74:75]
	v_add_co_u32_e32 v76, vcc, s72, v196
	v_cvt_pk_bf16_f32 v64, v64, v65
	v_cvt_pk_bf16_f32 v65, v66, v67
	v_cvt_pk_bf16_f32 v66, v72, v73
	v_cvt_pk_bf16_f32 v67, v74, v75
	v_addc_co_u32_e32 v77, vcc, 0, v197, vcc
	global_store_dwordx4 v[76:77], v[64:67], off offset:2048
	v_pk_mul_f32 v[72:73], v[94:95], v[230:231] op_sel_hi:[1,0]
	v_pk_mul_f32 v[74:75], v[192:193], v[230:231] op_sel_hi:[1,0]
	v_pk_mul_f32 v[66:67], v[92:93], v[230:231] op_sel_hi:[1,0]
	s_waitcnt vmcnt(9)
	v_lshlrev_b32_e32 v64, 16, v172
	v_and_b32_e32 v65, 0xffff0000, v172
	s_waitcnt lgkmcnt(1)
	v_pk_mul_f32 v[66:67], v[80:81], v[66:67]
	v_pk_mul_f32 v[72:73], v[82:83], v[72:73]
	v_pk_mul_f32 v[64:65], v[66:67], v[64:65]
	v_lshlrev_b32_e32 v66, 16, v173
	v_and_b32_e32 v67, 0xffff0000, v173
	v_pk_mul_f32 v[66:67], v[72:73], v[66:67]
	v_lshlrev_b32_e32 v72, 16, v174
	v_and_b32_e32 v73, 0xffff0000, v174
	s_waitcnt lgkmcnt(0)
	v_pk_mul_f32 v[74:75], v[84:85], v[74:75]
	v_pk_mul_f32 v[78:79], v[194:195], v[230:231] op_sel_hi:[1,0]
	v_pk_mul_f32 v[72:73], v[74:75], v[72:73]
	v_lshlrev_b32_e32 v74, 16, v175
	v_and_b32_e32 v75, 0xffff0000, v175
	v_pk_mul_f32 v[78:79], v[86:87], v[78:79]
	v_cvt_pk_bf16_f32 v64, v64, v65
	v_pk_mul_f32 v[74:75], v[78:79], v[74:75]
	v_cvt_pk_bf16_f32 v65, v66, v67
	v_cvt_pk_bf16_f32 v66, v72, v73
	v_cvt_pk_bf16_f32 v67, v74, v75
	global_store_dwordx4 v[76:77], v[64:67], off offset:2064
	ds_read_b128 v[64:67], v208 offset:64
	ds_read_b128 v[72:75], v208 offset:80
	v_pk_mul_f32 v[68:69], v[68:69], v[230:231] op_sel_hi:[1,0]
	v_pk_mul_f32 v[70:71], v[70:71], v[230:231] op_sel_hi:[1,0]
	v_lshlrev_b32_e32 v78, 16, v168
	s_waitcnt lgkmcnt(1)
	v_pk_mul_f32 v[64:65], v[64:65], v[68:69]
	v_lshlrev_b32_e32 v68, 16, v169
	v_and_b32_e32 v69, 0xffff0000, v169
	v_pk_mul_f32 v[66:67], v[66:67], v[70:71]
	v_pk_mul_f32 v[70:71], v[198:199], v[230:231] op_sel_hi:[1,0]
	v_pk_mul_f32 v[66:67], v[66:67], v[68:69]
	v_lshlrev_b32_e32 v68, 16, v170
	v_and_b32_e32 v69, 0xffff0000, v170
	s_waitcnt lgkmcnt(0)
	v_pk_mul_f32 v[70:71], v[72:73], v[70:71]
	v_pk_mul_f32 v[72:73], v[200:201], v[230:231] op_sel_hi:[1,0]
	v_and_b32_e32 v79, 0xffff0000, v168
	v_pk_mul_f32 v[68:69], v[70:71], v[68:69]
	v_lshlrev_b32_e32 v70, 16, v171
	v_and_b32_e32 v71, 0xffff0000, v171
	v_pk_mul_f32 v[72:73], v[74:75], v[72:73]
	v_pk_mul_f32 v[64:65], v[64:65], v[78:79]
	v_pk_mul_f32 v[70:71], v[72:73], v[70:71]
	v_cvt_pk_bf16_f32 v64, v64, v65
	v_cvt_pk_bf16_f32 v65, v66, v67
	v_cvt_pk_bf16_f32 v66, v68, v69
	v_cvt_pk_bf16_f32 v67, v70, v71
	global_store_dwordx4 v[76:77], v[64:67], off offset:2080
	ds_read_b128 v[64:67], v208 offset:96
	ds_read_b128 v[68:71], v208 offset:112
	v_pk_mul_f32 v[74:75], v[222:223], v[230:231] op_sel_hi:[1,0]
	v_lshlrev_b32_e32 v72, 16, v164
	v_and_b32_e32 v73, 0xffff0000, v164
	s_waitcnt lgkmcnt(1)
	v_pk_mul_f32 v[64:65], v[74:75], v[64:65]
	v_pk_mul_f32 v[74:75], v[224:225], v[230:231] op_sel_hi:[1,0]
	v_pk_mul_f32 v[64:65], v[64:65], v[72:73]
	v_lshlrev_b32_e32 v72, 16, v165
	v_and_b32_e32 v73, 0xffff0000, v165
	v_pk_mul_f32 v[66:67], v[74:75], v[66:67]
	v_pk_mul_f32 v[74:75], v[226:227], v[230:231] op_sel_hi:[1,0]
	v_pk_mul_f32 v[66:67], v[66:67], v[72:73]
	v_lshlrev_b32_e32 v72, 16, v166
	v_and_b32_e32 v73, 0xffff0000, v166
	s_waitcnt lgkmcnt(0)
	v_pk_mul_f32 v[68:69], v[74:75], v[68:69]
	v_pk_mul_f32 v[74:75], v[228:229], v[230:231] op_sel_hi:[1,0]
	v_pk_mul_f32 v[68:69], v[68:69], v[72:73]
	v_lshlrev_b32_e32 v72, 16, v167
	v_and_b32_e32 v73, 0xffff0000, v167
	v_pk_mul_f32 v[70:71], v[74:75], v[70:71]
	v_cvt_pk_bf16_f32 v64, v64, v65
	v_pk_mul_f32 v[70:71], v[70:71], v[72:73]
	v_cvt_pk_bf16_f32 v65, v66, v67
	v_cvt_pk_bf16_f32 v66, v68, v69
	v_cvt_pk_bf16_f32 v67, v70, v71
	global_store_dwordx4 v[76:77], v[64:67], off offset:2096
	s_cbranch_scc0 .LBB0_1712

; #define LAS __attribute__((address_space(3)))
; __device__ __forceinline__ void gla_unit(LAS unsigned char* lds, const unsigned char* ws, const float* g_onorm, const int b, const int h, const int wv) {
;     ...
;         f32x16 O[2];
; #pragma unroll
;         for (int tt = 0; tt < 2; ++tt)
; #pragma unroll
;             for (int r = 0; r < 16; ++r) O[tt][r] = 0.f;
; #pragma unroll
;         for (int et = 0; et < 4; ++et)
; #pragma unroll
;             for (int s2 = 0; s2 < 2; ++s2) {
;                 const bf16x8 sb = pack8(S[et], s2);
; #pragma unroll
;                 for (int tt = 0; tt < 2; ++tt) {
;                     const bf16x8 aq = ld2x64(qb8 + 32 * tt * QS + (32 * et + 16 * s2) * 2);
;                     O[tt] = __builtin_amdgcn_mfma_f32_32x32x16_bf16(aq, sb, O[tt], 0, 0, 0);
;                 }
;             }
;         __syncthreads();
; #pragma unroll
;         for (int pr = 0; pr < 3; ++pr) {
;             const int st = (pr == 2) ? 1 : 0, tt = (pr == 0) ? 0 : 1;
; #pragma unroll
;             for (int s2 = 0; s2 < 2; ++s2) {
;                 const bf16x8 ax = *(const LAS bf16x8*)(frb + (pr * 2 + s2) * 1024);
;                 const LAS unsigned char* vp = vP + (32 * st + 16 * s2) * VS;
;                 const bf16x8 bv = tr8(vp, vp + 8 * VS);
;                 O[tt] = __builtin_amdgcn_mfma_f32_32x32x16_bf16(ax, bv, O[tt], 0, 0, 0);
;             }
;         }
;         __builtin_amdgcn_sched_barrier(0);
; #pragma unroll
;         for (int tt = 0; tt < 2; ++tt)
; #pragma unroll
;             for (int r = 0; r < 16; ++r) ob[(32 * tt + (r & 3) + 8 * (r >> 2)) * OS] = O[tt][r];
;         __builtin_amdgcn_sched_barrier(0);
; #pragma unroll
;         for (int et = 0; et < 4; ++et)
; #pragma unroll
;             for (int rg = 0; rg < 4; ++rg) { const f32x4 dl = *(const LAS f32x4*)&decb[32 * et + 8 * rg];
.LBB0_1703:
	v_add_u32_e32 v222, v203, v202
	ds_read2_b64 v[64:67], v222 offset1:2
	v_cvt_pk_bf16_f32 v68, v48, v49
	v_cvt_pk_bf16_f32 v69, v50, v51
	v_cvt_pk_bf16_f32 v70, v52, v53
	v_cvt_pk_bf16_f32 v71, v54, v55
	v_add_u32_e32 v223, 0x2000, v222
	ds_read2_b64 v[228:231], v222 offset0:4 offset1:6
	v_cvt_pk_bf16_f32 v232, v56, v57
	v_cvt_pk_bf16_f32 v233, v58, v59
	s_waitcnt lgkmcnt(1)
	v_mfma_f32_32x32x16_bf16 v[80:95], v[64:67], v[68:71], 0
	ds_read2_b64 v[64:67], v223 offset0:64 offset1:66
	v_cvt_pk_bf16_f32 v234, v60, v61
	v_cvt_pk_bf16_f32 v235, v62, v63
	s_waitcnt lgkmcnt(1)
	s_nop 0
	v_mfma_f32_32x32x16_bf16 v[80:95], v[228:231], v[232:235], v[80:95]
	ds_read2_b64 v[228:231], v223 offset0:68 offset1:70
	s_waitcnt lgkmcnt(1)
	v_mfma_f32_32x32x16_bf16 v[64:79], v[64:67], v[68:71], 0
	s_waitcnt lgkmcnt(0)
	v_mfma_f32_32x32x16_bf16 v[64:79], v[228:231], v[232:235], v[64:79]
	ds_read2_b64 v[228:231], v222 offset0:8 offset1:10
	ds_read2_b64 v[236:239], v223 offset0:72 offset1:74
	ds_read2_b64 v[240:243], v222 offset0:12 offset1:14
	v_cvt_pk_bf16_f32 v232, v16, v17
	v_cvt_pk_bf16_f32 v233, v18, v19
	v_cvt_pk_bf16_f32 v234, v20, v21
	v_cvt_pk_bf16_f32 v235, v22, v23
	s_waitcnt lgkmcnt(2)
	s_nop 0
	v_mfma_f32_32x32x16_bf16 v[80:95], v[228:231], v[232:235], v[80:95]
	ds_read2_b64 v[248:251], v223 offset0:76 offset1:78
	s_waitcnt lgkmcnt(2)
	v_mfma_f32_32x32x16_bf16 v[64:79], v[236:239], v[232:235], v[64:79]
	ds_read2_b64 v[228:231], v222 offset0:16 offset1:18
	v_cvt_pk_bf16_f32 v232, v24, v25
	v_cvt_pk_bf16_f32 v233, v26, v27
	v_cvt_pk_bf16_f32 v234, v28, v29
	v_cvt_pk_bf16_f32 v235, v30, v31
	s_waitcnt lgkmcnt(2)
	s_nop 0
	v_mfma_f32_32x32x16_bf16 v[80:95], v[240:243], v[232:235], v[80:95]
	ds_read2_b64 v[236:239], v223 offset0:80 offset1:82
	s_waitcnt lgkmcnt(2)
	v_mfma_f32_32x32x16_bf16 v[64:79], v[248:251], v[232:235], v[64:79]
	ds_read2_b64 v[240:243], v222 offset0:20 offset1:22
	v_cvt_pk_bf16_f32 v232, v32, v33
	v_cvt_pk_bf16_f32 v233, v34, v35
	v_cvt_pk_bf16_f32 v234, v36, v37
	v_cvt_pk_bf16_f32 v235, v38, v39
	s_waitcnt lgkmcnt(2)
	s_nop 0
	v_mfma_f32_32x32x16_bf16 v[80:95], v[228:231], v[232:235], v[80:95]
	ds_read2_b64 v[248:251], v223 offset0:84 offset1:86
	s_waitcnt lgkmcnt(2)
	v_mfma_f32_32x32x16_bf16 v[64:79], v[236:239], v[232:235], v[64:79]
	ds_read2_b64 v[228:231], v222 offset0:24 offset1:26
	v_cvt_pk_bf16_f32 v232, v40, v41
	v_cvt_pk_bf16_f32 v233, v42, v43
	v_cvt_pk_bf16_f32 v234, v44, v45
	v_cvt_pk_bf16_f32 v235, v46, v47
	s_waitcnt lgkmcnt(2)
	s_nop 0
	v_mfma_f32_32x32x16_bf16 v[80:95], v[240:243], v[232:235], v[80:95]
	ds_read2_b64 v[236:239], v223 offset0:88 offset1:90
	s_waitcnt lgkmcnt(2)
	v_mfma_f32_32x32x16_bf16 v[64:79], v[248:251], v[232:235], v[64:79]
	ds_read2_b64 v[240:243], v222 offset0:28 offset1:30
	v_cvt_pk_bf16_f32 v232, v0, v1
	v_cvt_pk_bf16_f32 v233, v2, v3
	v_cvt_pk_bf16_f32 v234, v4, v5
	v_cvt_pk_bf16_f32 v235, v6, v7
	s_waitcnt lgkmcnt(2)
	s_nop 0
	v_mfma_f32_32x32x16_bf16 v[80:95], v[228:231], v[232:235], v[80:95]
	ds_read2_b64 v[248:251], v223 offset0:92 offset1:94
	s_waitcnt lgkmcnt(2)
	v_mfma_f32_32x32x16_bf16 v[64:79], v[236:239], v[232:235], v[64:79]
	v_cvt_pk_bf16_f32 v232, v8, v9
	v_cvt_pk_bf16_f32 v233, v10, v11
	v_cvt_pk_bf16_f32 v234, v12, v13
	v_cvt_pk_bf16_f32 v235, v14, v15
	s_waitcnt lgkmcnt(1)
	s_nop 0
	v_mfma_f32_32x32x16_bf16 v[80:95], v[240:243], v[232:235], v[80:95]
	s_waitcnt lgkmcnt(0)
	s_barrier
	v_mfma_f32_32x32x16_bf16 v[64:79], v[248:251], v[232:235], v[64:79]
	ds_read_b128 v[228:231], v206
	ds_read_b64_tr_b16 v[232:233], v218
	ds_read_b64_tr_b16 v[234:235], v218 offset:4608
	ds_read_b128 v[236:239], v206 offset:1024
	ds_read_b64_tr_b16 v[240:241], v218 offset:9216
	ds_read_b64_tr_b16 v[242:243], v218 offset:13824
	s_waitcnt lgkmcnt(3)
	v_mfma_f32_32x32x16_bf16 v[80:95], v[228:231], v[232:235], v[80:95]
	s_waitcnt lgkmcnt(0)
	v_mfma_f32_32x32x16_bf16 v[80:95], v[236:239], v[240:243], v[80:95]
	ds_read_b128 v[228:231], v206 offset:2048
	ds_read_b128 v[236:239], v206 offset:3072
	s_waitcnt lgkmcnt(1)
	v_mfma_f32_32x32x16_bf16 v[64:79], v[228:231], v[232:235], v[64:79]
	s_waitcnt lgkmcnt(0)
	v_mfma_f32_32x32x16_bf16 v[64:79], v[236:239], v[240:243], v[64:79]
	ds_read_b128 v[228:231], v206 offset:4096
	ds_read_b64_tr_b16 v[232:233], v218 offset:18432
	ds_read_b64_tr_b16 v[234:235], v218 offset:23040
	ds_read_b128 v[236:239], v206 offset:5120
	ds_read_b64_tr_b16 v[240:241], v218 offset:27648
	ds_read_b64_tr_b16 v[242:243], v218 offset:32256
	s_waitcnt lgkmcnt(3)
	v_mfma_f32_32x32x16_bf16 v[64:79], v[228:231], v[232:235], v[64:79]
	s_waitcnt lgkmcnt(0)
	v_mfma_f32_32x32x16_bf16 v[64:79], v[236:239], v[240:243], v[64:79]
	ds_write_b32 v207, v80
	ds_write_b32 v207, v81 offset:1040
	ds_write_b32 v207, v82 offset:2080
	ds_write_b32 v207, v83 offset:3120
	ds_write_b32 v207, v84 offset:8320
	ds_write_b32 v207, v85 offset:9360
	ds_write_b32 v207, v86 offset:10400
	ds_write_b32 v207, v87 offset:11440
	ds_write_b32 v207, v88 offset:16640
	ds_write_b32 v207, v89 offset:17680
	ds_write_b32 v207, v90 offset:18720
	ds_write_b32 v207, v91 offset:19760
	ds_write_b32 v207, v92 offset:24960
	ds_write_b32 v207, v93 offset:26000
	ds_write_b32 v207, v94 offset:27040
	ds_write_b32 v207, v95 offset:28080
	ds_write_b32 v207, v64 offset:33280
	ds_write_b32 v207, v65 offset:34320
	ds_write_b32 v207, v66 offset:35360
	ds_write_b32 v207, v67 offset:36400
	ds_write_b32 v207, v68 offset:41600
	ds_write_b32 v207, v69 offset:42640
	ds_write_b32 v207, v70 offset:43680
	ds_write_b32 v207, v71 offset:44720
	ds_write_b32 v207, v72 offset:49920
	ds_write_b32 v207, v73 offset:50960
	ds_write_b32 v207, v74 offset:52000
	ds_write_b32 v207, v75 offset:53040
	ds_write_b32 v207, v76 offset:58240
	ds_write_b32 v207, v77 offset:59280
	ds_write_b32 v207, v78 offset:60320
	ds_write_b32 v207, v79 offset:61360
	ds_read_b128 v[64:67], v205 offset:96
	ds_read_b128 v[68:71], v205 offset:64
	ds_read_b128 v[72:75], v205 offset:32
	ds_read_b128 v[76:79], v205
	s_waitcnt vmcnt(11)
; #define LAS __attribute__((address_space(3)))
; __device__ __forceinline__ void gla_unit(LAS unsigned char* lds, const unsigned char* ws, const float* g_onorm, const int b, const int h, const int wv) {
;     ...
; #pragma unroll
;         for (int et = 0; et < 4; ++et)
; #pragma unroll
;             for (int rg = 0; rg < 4; ++rg) { const f32x4 dl = *(const LAS f32x4*)&decb[32 * et + 8 * rg];
; #pragma unroll
;                 for (int x = 0; x < 4; ++x) S[et][4 * rg + x] *= dl[x]; }
; #pragma unroll
;         for (int ks = 0; ks < 4; ++ks) {
;             const LAS unsigned char* vp = vN + 16 * ks * VS;
;             const bf16x8 bv = tr8(vp, vp + 4 * VS);
; #pragma unroll
;             for (int et = 0; et < 4; ++et) {
;                 const LAS unsigned char* kp = keN + 32 * et * 2 + 16 * ks * ES;
;                 const bf16x8 ak = tr8(kp, kp + 4 * ES);
;                 S[et] = __builtin_amdgcn_mfma_f32_32x32x16_bf16(ak, bv, S[et], 0, 0, 0);
;             }
;         }
	v_lshlrev_b32_e32 v246, 16, v176
	s_waitcnt lgkmcnt(3)
	v_pk_mul_f32 v[62:63], v[62:63], v[66:67]
	s_waitcnt lgkmcnt(2)
	v_pk_mul_f32 v[58:59], v[58:59], v[70:71]
	v_pk_mul_f32 v[60:61], v[60:61], v[64:65]
	s_waitcnt lgkmcnt(0)
	v_pk_mul_f32 v[50:51], v[50:51], v[78:79]
	v_pk_mul_f32 v[56:57], v[56:57], v[68:69]
	ds_read_b128 v[64:67], v205 offset:192
	ds_read_b128 v[68:71], v205 offset:224
	ds_read_b128 v[78:81], v205 offset:128
	ds_read_b128 v[82:85], v205 offset:160
	v_pk_mul_f32 v[54:55], v[54:55], v[74:75]
	v_pk_mul_f32 v[52:53], v[52:53], v[72:73]
	v_pk_mul_f32 v[48:49], v[48:49], v[76:77]
	s_waitcnt lgkmcnt(2)
	v_pk_mul_f32 v[30:31], v[30:31], v[70:71]
	v_pk_mul_f32 v[26:27], v[26:27], v[66:67]
	s_waitcnt lgkmcnt(0)
	v_pk_mul_f32 v[22:23], v[22:23], v[84:85]
	v_pk_mul_f32 v[18:19], v[18:19], v[80:81]
	v_pk_mul_f32 v[28:29], v[28:29], v[68:69]
	v_pk_mul_f32 v[24:25], v[24:25], v[64:65]
	v_pk_mul_f32 v[20:21], v[20:21], v[82:83]
	ds_read_b128 v[64:67], v205 offset:256
	ds_read_b128 v[68:71], v205 offset:288
	ds_read_b128 v[72:75], v205 offset:320
	ds_read_b128 v[80:83], v205 offset:352
	ds_read_b64_tr_b16 v[84:85], v219
	ds_read_b64_tr_b16 v[86:87], v219 offset:2304
	ds_read_b64_tr_b16 v[90:91], v220 offset:1280
	ds_read_b64_tr_b16 v[88:89], v220
	ds_read_b64_tr_b16 v[92:93], v220 offset:64
	ds_read_b64_tr_b16 v[228:229], v220 offset:128
	ds_read_b64_tr_b16 v[232:233], v220 offset:192
	ds_read_b64_tr_b16 v[94:95], v220 offset:1344
	ds_read_b64_tr_b16 v[230:231], v220 offset:1408
	ds_read_b64_tr_b16 v[234:235], v220 offset:1472
	ds_read_b64_tr_b16 v[236:237], v219 offset:9216
	ds_read_b64_tr_b16 v[238:239], v219 offset:11520
	s_waitcnt lgkmcnt(8)
	v_mfma_f32_32x32x16_bf16 v[48:63], v[88:91], v[84:87], v[48:63]
	v_mul_f32_e64 v16, v16, v78
	v_mul_f32_e64 v17, v17, v79
	v_mul_f32_e64 v42, v42, v74
	v_mul_f32_e64 v43, v43, v75
	v_mul_f32_e64 v38, v38, v70
	v_mul_f32_e64 v39, v39, v71
	v_pk_mul_f32 v[34:35], v[34:35], v[66:67]
	v_pk_mul_f32 v[44:45], v[44:45], v[80:81]
	v_pk_mul_f32 v[40:41], v[40:41], v[72:73]
	ds_read_b128 v[70:73], v205 offset:448
	ds_read_b128 v[74:77], v205 offset:480
	v_pk_mul_f32 v[36:37], v[36:37], v[68:69]
	ds_read_b128 v[66:69], v205 offset:384
	ds_read_b128 v[78:81], v205 offset:416
	v_pk_mul_f32 v[46:47], v[46:47], v[82:83]
	v_pk_mul_f32 v[32:33], v[32:33], v[64:65]
	s_waitcnt lgkmcnt(2)
	v_pk_mul_f32 v[14:15], v[14:15], v[76:77]
	v_pk_mul_f32 v[10:11], v[10:11], v[72:73]
	s_waitcnt lgkmcnt(0)
	v_pk_mul_f32 v[6:7], v[6:7], v[80:81]
	v_pk_mul_f32 v[2:3], v[2:3], v[68:69]
	v_pk_mul_f32 v[12:13], v[12:13], v[74:75]
	v_pk_mul_f32 v[8:9], v[8:9], v[70:71]
	v_pk_mul_f32 v[4:5], v[4:5], v[78:79]
	v_pk_mul_f32 v[0:1], v[0:1], v[66:67]
	v_mfma_f32_32x32x16_bf16 v[16:31], v[92:95], v[84:87], v[16:31]
	ds_read_b64_tr_b16 v[66:67], v220 offset:6400
	ds_read_b64_tr_b16 v[64:65], v220 offset:5120
	ds_read_b64_tr_b16 v[68:69], v220 offset:5184
	ds_read_b64_tr_b16 v[72:73], v220 offset:5248
	ds_read_b64_tr_b16 v[76:77], v220 offset:5312
	ds_read_b64_tr_b16 v[70:71], v220 offset:6464
	ds_read_b64_tr_b16 v[74:75], v220 offset:6528
	ds_read_b64_tr_b16 v[78:79], v220 offset:6592
	v_and_b32_e32 v247, 0xffff0000, v176
	v_mfma_f32_32x32x16_bf16 v[32:47], v[228:231], v[84:87], v[32:47]
	v_mfma_f32_32x32x16_bf16 v[0:15], v[232:235], v[84:87], v[0:15]
	s_waitcnt lgkmcnt(6)
	v_mfma_f32_32x32x16_bf16 v[48:63], v[64:67], v[236:239], v[48:63]
	s_waitcnt lgkmcnt(2)
	v_mfma_f32_32x32x16_bf16 v[16:31], v[68:71], v[236:239], v[16:31]
	s_waitcnt lgkmcnt(1)
	v_mfma_f32_32x32x16_bf16 v[32:47], v[72:75], v[236:239], v[32:47]
	s_waitcnt lgkmcnt(0)
	v_mfma_f32_32x32x16_bf16 v[0:15], v[76:79], v[236:239], v[0:15]
	ds_read_b64_tr_b16 v[64:65], v219 offset:18432
	ds_read_b64_tr_b16 v[66:67], v219 offset:20736
	ds_read_b64_tr_b16 v[70:71], v220 offset:11520
	ds_read_b64_tr_b16 v[68:69], v220 offset:10240
	ds_read_b64_tr_b16 v[72:73], v220 offset:10304
	ds_read_b64_tr_b16 v[76:77], v220 offset:10368
	ds_read_b64_tr_b16 v[80:81], v220 offset:10432
	ds_read_b64_tr_b16 v[74:75], v220 offset:11584
	ds_read_b64_tr_b16 v[78:79], v220 offset:11648
	ds_read_b64_tr_b16 v[82:83], v220 offset:11712
	ds_read_b64_tr_b16 v[84:85], v219 offset:27648
	ds_read_b64_tr_b16 v[86:87], v219 offset:29952
	s_waitcnt lgkmcnt(8)
	v_mfma_f32_32x32x16_bf16 v[48:63], v[68:71], v[64:67], v[48:63]
	ds_read_b64_tr_b16 v[68:69], v220 offset:16640
	s_waitcnt lgkmcnt(5)
	v_mfma_f32_32x32x16_bf16 v[16:31], v[72:75], v[64:67], v[16:31]
	s_waitcnt lgkmcnt(4)
	v_mfma_f32_32x32x16_bf16 v[32:47], v[76:79], v[64:67], v[32:47]
	s_waitcnt lgkmcnt(3)
	v_mfma_f32_32x32x16_bf16 v[0:15], v[80:83], v[64:67], v[0:15]
	ds_read_b64_tr_b16 v[66:67], v220 offset:15360
	ds_read_b64_tr_b16 v[70:71], v220 offset:15424
	ds_read_b64_tr_b16 v[74:75], v220 offset:15488
	ds_read_b64_tr_b16 v[78:79], v220 offset:15552
	ds_read_b64_tr_b16 v[72:73], v220 offset:16704
	ds_read_b64_tr_b16 v[76:77], v220 offset:16768
	ds_read_b64_tr_b16 v[80:81], v220 offset:16832
	s_waitcnt lgkmcnt(0)
	s_barrier
; #define LAS __attribute__((address_space(3)))
; __device__ __forceinline__ unsigned cvt_pk_bf16(float lo, float hi) { const bf16x2_t r = __builtin_convertvector((f32x2_t){lo, hi}, bf16x2_t); return __builtin_bit_cast(unsigned, r); }
; __device__ __forceinline__ void gla_unit(LAS unsigned char* lds, const unsigned char* ws, const float* g_onorm, const int b, const int h, const int wv) {
;     ...
;                 S[et] = __builtin_amdgcn_mfma_f32_32x32x16_bf16(ak, bv, S[et], 0, 0, 0);
;             }
;         }
;         __syncthreads();
;         {
;             const int t = tid >> 3, g8 = tid & 7;
;             float ov[32]; float ss = 0.f;
; #pragma unroll
;             for (int x = 0; x < 8; ++x) { const f32x4 v = *(const LAS f32x4*)&obuf[t * OS + 32 * g8 + 4 * x]; ov[4 * x] = v[0]; ov[4 * x + 1] = v[1]; ov[4 * x + 2] = v[2]; ov[4 * x + 3] = v[3];
;                 ss += v[0] * v[0] + v[1] * v[1] + v[2] * v[2] + v[3] * v[3]; }
;             ss += __builtin_bit_cast(float, __builtin_amdgcn_ds_swizzle(__builtin_bit_cast(int, ss), (1 << 10) | 0x1F)); ss += __builtin_bit_cast(float, __builtin_amdgcn_ds_swizzle(__builtin_bit_cast(int, ss), (2 << 10) | 0x1F));
;             ss += __builtin_bit_cast(float, __builtin_amdgcn_ds_swizzle(__builtin_bit_cast(int, ss), (4 << 10) | 0x1F));
;             const float rstd = __builtin_amdgcn_rsqf(ss * (1.0f / 256.0f) + EPSV);
;             bf16_t* mp = mix + (t0 + t) * DM + 1024 + h * 256 + 32 * g8;
; #pragma unroll
;             for (int x = 0; x < 4; ++x) {
;                 const u32x4 og = ogr[x];
;                 const f32x4 g0 = *(const LAS f32x4*)&gon[32 * g8 + 8 * x], g1 = *(const LAS f32x4*)&gon[32 * g8 + 8 * x + 4];
;                 const float gg2[8] = {g0[0], g0[1], g0[2], g0[3], g1[0], g1[1], g1[2], g1[3]};
;                 float res[8];
; #pragma unroll
;                 for (int y = 0; y < 4; ++y) { const float a0 = bf_lo(og[y]), a1 = bf_hi(og[y]);
;                     res[2 * y] = ov[8 * x + 2 * y] * rstd * gg2[2 * y] * a0;
;                     res[2 * y + 1] = ov[8 * x + 2 * y + 1] * rstd * gg2[2 * y + 1] * a1; }
;                 u32x4 wv4; wv4[0] = cvt_pk_bf16(res[0], res[1]); wv4[1] = cvt_pk_bf16(res[2], res[3]); wv4[2] = cvt_pk_bf16(res[4], res[5]); wv4[3] = cvt_pk_bf16(res[6], res[7]);
;                 *(u32x4*)(mp + 8 * x) = wv4;
;             }
	v_mfma_f32_32x32x16_bf16 v[48:63], v[66:69], v[84:87], v[48:63]
	ds_read_b128 v[64:67], v221
	ds_read_b128 v[88:91], v221 offset:16
	ds_read_b128 v[92:95], v221 offset:32
	ds_read_b128 v[228:231], v221 offset:48
	s_waitcnt lgkmcnt(3)
	v_mul_f32_e32 v68, v65, v65
	s_waitcnt lgkmcnt(2)
	v_mul_f32_e32 v69, v89, v89
	v_fmac_f32_e32 v68, v64, v64
	v_fmac_f32_e32 v69, v88, v88
	v_fmac_f32_e32 v68, v66, v66
	v_fmac_f32_e32 v69, v90, v90
	v_mfma_f32_32x32x16_bf16 v[16:31], v[70:73], v[84:87], v[16:31]
	v_fmac_f32_e32 v68, v67, v67
	v_fmac_f32_e32 v69, v91, v91
	s_waitcnt lgkmcnt(1)
	v_mov_b32_e32 v70, v93
	s_waitcnt lgkmcnt(0)
	v_mov_b32_e32 v71, v229
	v_add_f32_e32 v196, v68, v69
	v_mov_b32_e32 v68, v92
	v_mov_b32_e32 v69, v228
	v_pk_mul_f32 v[70:71], v[70:71], v[70:71]
	v_mov_b32_e32 v82, v95
	v_pk_fma_f32 v[68:69], v[68:69], v[68:69], v[70:71]
	v_mov_b32_e32 v70, v94
	v_mov_b32_e32 v71, v230
	v_pk_fma_f32 v[72:73], v[70:71], v[70:71], v[68:69]
	ds_read_b128 v[68:71], v221 offset:64
	ds_read_b128 v[232:235], v221 offset:80
	v_mov_b32_e32 v83, v231
	v_pk_fma_f32 v[72:73], v[82:83], v[82:83], v[72:73]
	ds_read_b128 v[236:239], v221 offset:96
	ds_read_b128 v[240:243], v221 offset:112
	v_add_f32_e32 v72, v196, v72
	s_waitcnt lgkmcnt(3)
	v_mov_b32_e32 v82, v69
	s_waitcnt lgkmcnt(2)
	v_mov_b32_e32 v83, v233
	v_add_f32_e32 v196, v72, v73
	v_mov_b32_e32 v72, v68
	v_mov_b32_e32 v73, v232
	v_pk_mul_f32 v[82:83], v[82:83], v[82:83]
	v_mfma_f32_32x32x16_bf16 v[32:47], v[74:77], v[84:87], v[32:47]
	v_fma_f32 v72, v72, v72, v82
	v_fma_f32 v73, v73, v73, v83
	v_mov_b32_e32 v82, v70
	v_mov_b32_e32 v83, v234
	v_fma_f32 v72, v82, v82, v72
	v_fma_f32 v73, v83, v83, v73
	v_mov_b32_e32 v82, v71
	v_mov_b32_e32 v83, v235
	v_pk_fma_f32 v[72:73], v[82:83], v[82:83], v[72:73]
	s_waitcnt lgkmcnt(1)
	v_mov_b32_e32 v82, v237
	v_add_f32_e32 v72, v196, v72
	s_waitcnt lgkmcnt(0)
	v_mov_b32_e32 v83, v241
	v_add_f32_e32 v196, v72, v73
	v_mov_b32_e32 v72, v236
	v_mov_b32_e32 v73, v240
	v_pk_mul_f32 v[82:83], v[82:83], v[82:83]
	v_mfma_f32_32x32x16_bf16 v[0:15], v[78:81], v[84:87], v[0:15]
	v_fma_f32 v72, v72, v72, v82
	v_fma_f32 v73, v73, v73, v83
	v_mov_b32_e32 v82, v238
	v_mov_b32_e32 v83, v242
	v_fma_f32 v72, v82, v82, v72
	v_fma_f32 v73, v83, v83, v73
	v_mov_b32_e32 v82, v239
	v_mov_b32_e32 v83, v243
	v_pk_fma_f32 v[72:73], v[82:83], v[82:83], v[72:73]
	s_nop 0
	v_add_f32_e32 v72, v196, v72
	v_add_f32_e32 v72, v72, v73
	ds_swizzle_b32 v73, v72 offset:swizzle(SWAP,1)
	v_lshl_add_u64 v[196:197], s[76:77], 0, v[188:189]
	s_waitcnt lgkmcnt(0)
	v_add_f32_e32 v72, v72, v73
	ds_swizzle_b32 v73, v72 offset:swizzle(SWAP,2)
	s_waitcnt lgkmcnt(0)
	v_add_f32_e32 v72, v72, v73
	ds_swizzle_b32 v73, v72 offset:swizzle(SWAP,4)
	s_waitcnt lgkmcnt(0)
	v_add_f32_e32 v72, v72, v73
	v_fmamk_f32 v72, v72, 0x3b800000, v181
	v_rsq_f32_e32 v244, v72
	ds_read_b128 v[72:75], v208
	ds_read_b128 v[76:79], v208 offset:16
	ds_read_b128 v[80:83], v208 offset:32
	ds_read_b128 v[84:87], v208 offset:48
	v_pk_mul_f32 v[64:65], v[64:65], v[244:245] op_sel_hi:[1,0]
	v_pk_mul_f32 v[66:67], v[66:67], v[244:245] op_sel_hi:[1,0]
	s_waitcnt lgkmcnt(3)
	v_pk_mul_f32 v[64:65], v[72:73], v[64:65]
	v_lshlrev_b32_e32 v72, 16, v177
	v_and_b32_e32 v73, 0xffff0000, v177
	v_pk_mul_f32 v[66:67], v[74:75], v[66:67]
	v_pk_mul_f32 v[74:75], v[88:89], v[244:245] op_sel_hi:[1,0]
	v_pk_mul_f32 v[66:67], v[66:67], v[72:73]
	v_lshlrev_b32_e32 v72, 16, v178
	v_and_b32_e32 v73, 0xffff0000, v178
	s_waitcnt lgkmcnt(2)
	v_pk_mul_f32 v[74:75], v[76:77], v[74:75]
	v_pk_mul_f32 v[76:77], v[90:91], v[244:245] op_sel_hi:[1,0]
	v_pk_mul_f32 v[72:73], v[74:75], v[72:73]
	v_lshlrev_b32_e32 v74, 16, v179
	v_and_b32_e32 v75, 0xffff0000, v179
	v_pk_mul_f32 v[76:77], v[78:79], v[76:77]
	v_pk_mul_f32 v[64:65], v[64:65], v[246:247]
	v_pk_mul_f32 v[74:75], v[76:77], v[74:75]
	v_add_co_u32_e32 v76, vcc, s33, v196
	v_cvt_pk_bf16_f32 v64, v64, v65
	v_cvt_pk_bf16_f32 v65, v66, v67
	v_cvt_pk_bf16_f32 v66, v72, v73
	v_cvt_pk_bf16_f32 v67, v74, v75
	v_addc_co_u32_e32 v77, vcc, 0, v197, vcc
	global_store_dwordx4 v[76:77], v[64:67], off offset:2048
	v_pk_mul_f32 v[72:73], v[94:95], v[244:245] op_sel_hi:[1,0]
	v_pk_mul_f32 v[74:75], v[228:229], v[244:245] op_sel_hi:[1,0]
	v_pk_mul_f32 v[66:67], v[92:93], v[244:245] op_sel_hi:[1,0]
	s_waitcnt vmcnt(9)
; #define LAS __attribute__((address_space(3)))
; __device__ __forceinline__ unsigned cvt_pk_bf16(float lo, float hi) { const bf16x2_t r = __builtin_convertvector((f32x2_t){lo, hi}, bf16x2_t); return __builtin_bit_cast(unsigned, r); }
; __device__ __forceinline__ float bf_lo(unsigned w) { return __uint_as_float(w << 16); }
; __device__ __forceinline__ float bf_hi(unsigned w) { return __uint_as_float(w & 0xffff0000u); }
; __device__ __forceinline__ void gla_unit(LAS unsigned char* lds, const unsigned char* ws, const float* g_onorm, const int b, const int h, const int wv) {
;     ...
;         __syncthreads();
; #pragma unroll
;         for (int i = 0; i < 2; ++i) { const int c = tid + 512 * i, row = c >> 4, cc = (c & 15) * 16;
;             *(LAS u32x4*)(lds + L_Q + row * QS + cc) = qr[par][i]; *(LAS u32x4*)(lds + L_K + row * QS + cc) = kr[par][i]; }
; #pragma unroll
;         for (int i = 0; i < 4; ++i) { const int c = tid + 512 * i; *(LAS u32x4*)(lds + L_V + (c >> 5) * VS + (c & 31) * 16) = vr[par][i]; }
;         if (tid < 32) {
;             const float L2E_ = 1.4426950408889634f;
;             *(LAS f32x4*)&dec[tid * 4] = (f32x4){__builtin_amdgcn_exp2f(dr[0] * L2E_), __builtin_amdgcn_exp2f(dr[1] * L2E_), __builtin_amdgcn_exp2f(dr[2] * L2E_), __builtin_amdgcn_exp2f(dr[3] * L2E_)};
;         }
;     ...
; #pragma unroll
;             for (int x = 0; x < 4; ++x) {
;                 const u32x4 og = ogr[x];
;                 const f32x4 g0 = *(const LAS f32x4*)&gon[32 * g8 + 8 * x], g1 = *(const LAS f32x4*)&gon[32 * g8 + 8 * x + 4];
;                 const float gg2[8] = {g0[0], g0[1], g0[2], g0[3], g1[0], g1[1], g1[2], g1[3]};
;                 float res[8];
; #pragma unroll
;                 for (int y = 0; y < 4; ++y) { const float a0 = bf_lo(og[y]), a1 = bf_hi(og[y]);
;                     res[2 * y] = ov[8 * x + 2 * y] * rstd * gg2[2 * y] * a0;
;                     res[2 * y + 1] = ov[8 * x + 2 * y + 1] * rstd * gg2[2 * y + 1] * a1; }
;                 u32x4 wv4; wv4[0] = cvt_pk_bf16(res[0], res[1]); wv4[1] = cvt_pk_bf16(res[2], res[3]); wv4[2] = cvt_pk_bf16(res[4], res[5]); wv4[3] = cvt_pk_bf16(res[6], res[7]);
;                 *(u32x4*)(mp + 8 * x) = wv4;
;             }
	v_lshlrev_b32_e32 v64, 16, v172
	v_and_b32_e32 v65, 0xffff0000, v172
	s_waitcnt lgkmcnt(1)
	v_pk_mul_f32 v[66:67], v[80:81], v[66:67]
	v_pk_mul_f32 v[72:73], v[82:83], v[72:73]
	v_pk_mul_f32 v[64:65], v[66:67], v[64:65]
	v_lshlrev_b32_e32 v66, 16, v173
	v_and_b32_e32 v67, 0xffff0000, v173
	v_pk_mul_f32 v[66:67], v[72:73], v[66:67]
	v_lshlrev_b32_e32 v72, 16, v174
	v_and_b32_e32 v73, 0xffff0000, v174
	s_waitcnt lgkmcnt(0)
	v_pk_mul_f32 v[74:75], v[84:85], v[74:75]
	v_pk_mul_f32 v[78:79], v[230:231], v[244:245] op_sel_hi:[1,0]
	v_pk_mul_f32 v[72:73], v[74:75], v[72:73]
	v_lshlrev_b32_e32 v74, 16, v175
	v_and_b32_e32 v75, 0xffff0000, v175
	v_pk_mul_f32 v[78:79], v[86:87], v[78:79]
	v_cvt_pk_bf16_f32 v64, v64, v65
	v_pk_mul_f32 v[74:75], v[78:79], v[74:75]
	v_cvt_pk_bf16_f32 v65, v66, v67
	v_cvt_pk_bf16_f32 v66, v72, v73
	v_cvt_pk_bf16_f32 v67, v74, v75
	global_store_dwordx4 v[76:77], v[64:67], off offset:2064
	ds_read_b128 v[64:67], v208 offset:64
	ds_read_b128 v[72:75], v208 offset:80
	v_pk_mul_f32 v[68:69], v[68:69], v[244:245] op_sel_hi:[1,0]
	v_pk_mul_f32 v[70:71], v[70:71], v[244:245] op_sel_hi:[1,0]
	v_lshlrev_b32_e32 v78, 16, v168
	s_waitcnt lgkmcnt(1)
	v_pk_mul_f32 v[64:65], v[64:65], v[68:69]
	v_lshlrev_b32_e32 v68, 16, v169
	v_and_b32_e32 v69, 0xffff0000, v169
	v_pk_mul_f32 v[66:67], v[66:67], v[70:71]
	v_pk_mul_f32 v[70:71], v[232:233], v[244:245] op_sel_hi:[1,0]
	v_pk_mul_f32 v[66:67], v[66:67], v[68:69]
	v_lshlrev_b32_e32 v68, 16, v170
	v_and_b32_e32 v69, 0xffff0000, v170
	s_waitcnt lgkmcnt(0)
	v_pk_mul_f32 v[70:71], v[72:73], v[70:71]
	v_pk_mul_f32 v[72:73], v[234:235], v[244:245] op_sel_hi:[1,0]
	v_and_b32_e32 v79, 0xffff0000, v168
	v_pk_mul_f32 v[68:69], v[70:71], v[68:69]
	v_lshlrev_b32_e32 v70, 16, v171
	v_and_b32_e32 v71, 0xffff0000, v171
	v_pk_mul_f32 v[72:73], v[74:75], v[72:73]
	v_pk_mul_f32 v[64:65], v[64:65], v[78:79]
	v_pk_mul_f32 v[70:71], v[72:73], v[70:71]
	v_cvt_pk_bf16_f32 v64, v64, v65
	v_cvt_pk_bf16_f32 v65, v66, v67
	v_cvt_pk_bf16_f32 v66, v68, v69
	v_cvt_pk_bf16_f32 v67, v70, v71
	global_store_dwordx4 v[76:77], v[64:67], off offset:2080
	ds_read_b128 v[64:67], v208 offset:96
	ds_read_b128 v[68:71], v208 offset:112
	v_pk_mul_f32 v[74:75], v[236:237], v[244:245] op_sel_hi:[1,0]
	v_lshlrev_b32_e32 v72, 16, v164
	v_and_b32_e32 v73, 0xffff0000, v164
	s_waitcnt lgkmcnt(1)
	v_pk_mul_f32 v[64:65], v[74:75], v[64:65]
	v_pk_mul_f32 v[74:75], v[238:239], v[244:245] op_sel_hi:[1,0]
	v_pk_mul_f32 v[64:65], v[64:65], v[72:73]
	v_lshlrev_b32_e32 v72, 16, v165
	v_and_b32_e32 v73, 0xffff0000, v165
	v_pk_mul_f32 v[66:67], v[74:75], v[66:67]
	v_pk_mul_f32 v[74:75], v[240:241], v[244:245] op_sel_hi:[1,0]
	v_pk_mul_f32 v[66:67], v[66:67], v[72:73]
	v_lshlrev_b32_e32 v72, 16, v166
	v_and_b32_e32 v73, 0xffff0000, v166
	s_waitcnt lgkmcnt(0)
	v_pk_mul_f32 v[68:69], v[74:75], v[68:69]
	v_pk_mul_f32 v[74:75], v[242:243], v[244:245] op_sel_hi:[1,0]
	v_pk_mul_f32 v[68:69], v[68:69], v[72:73]
	v_lshlrev_b32_e32 v72, 16, v167
	v_and_b32_e32 v73, 0xffff0000, v167
	v_pk_mul_f32 v[70:71], v[74:75], v[70:71]
	v_cvt_pk_bf16_f32 v64, v64, v65
	v_pk_mul_f32 v[70:71], v[70:71], v[72:73]
	v_cvt_pk_bf16_f32 v65, v66, v67
	v_cvt_pk_bf16_f32 v66, v68, v69
	v_cvt_pk_bf16_f32 v67, v70, v71
	global_store_dwordx4 v[76:77], v[64:67], off offset:2096
	s_barrier
	s_waitcnt vmcnt(20)
	ds_write_b128 v209, v[132:135]
	ds_write_b128 v209, v[136:139] offset:17408
	ds_write_b128 v210, v[140:143]
	ds_write_b128 v210, v[144:147] offset:17408
	ds_write_b128 v211, v[148:151]
	ds_write_b128 v212, v[152:155]
	ds_write_b128 v213, v[156:159]
	ds_write_b128 v214, v[160:163]
	s_and_saveexec_b64 s[42:43], s[0:1]
	s_cbranch_execz .LBB0_1705
	s_waitcnt vmcnt(12)
	v_mul_f32_e32 v64, 0x3fb8aa3b, v128
	v_mul_f32_e32 v65, 0x3fb8aa3b, v129
	v_mul_f32_e32 v66, 0x3fb8aa3b, v130
	v_mul_f32_e32 v67, 0x3fb8aa3b, v131
	v_exp_f32_e32 v64, v64
	v_exp_f32_e32 v65, v65
	v_exp_f32_e32 v66, v66
	v_exp_f32_e32 v67, v67
	ds_write_b128 v226, v[64:67]
